# P10 VALU cuts: high plane masked on the permute results (4 perm + 4 and per pair-dword), coefficient pairs packed in a VGPR (one readlane per pair), rows fetched by buffer loads with the row offset in
# speedup vs baseline: 1.0515x; 1.0277x over previous
; #define EXP_ROW(src, l) (*(const u32x4*)(UV + ((unsigned)__builtin_amdgcn_readlane((src), (l)) * 1024u + lo16)))
; #define EXP_XROW(tt) do { const char* g_ = (const char*)(xin + (size_t)(tt) * 1024) + lane * 16; LAS unsigned char* l_ = xslot + ((tt) & 1) * 2048; \
;         __builtin_amdgcn_global_load_lds((const unsigned*)g_, (LAS unsigned*)l_, 16, 0, 2); __builtin_amdgcn_global_load_lds((const unsigned*)(g_ + 1024), (LAS unsigned*)(l_ + 1024), 16, 0, 2); } while (0)
; __device__ __forceinline__ void expert_tokens(const unsigned char* __restrict__ UV, const float* __restrict__ US, const float* __restrict__ VS, ...
;     if (t0 >= t1) return;
;     const unsigned lo16 = (unsigned)lane * 16u;
;     const int el = ((lane >> 5) & 1) * 8 + ((lane >> 4) & 1) * 4 + ((lane >> 1) & 1) * 2 + (lane & 1);
;     const unsigned cw0 = (unsigned)IDX[(size_t)t0 * 128 + lane], cw1 = (unsigned)IDX[(size_t)t0 * 128 + 64 + lane];
;     int ci0 = (int)cw0 & rmask, ci1 = (int)cw1 & rmask;
;     float cg0 = __uint_as_float(cw0 & 0xFFFF0000u), cg1 = __uint_as_float(cw1 & 0xFFFF0000u);
;     float csu0 = US[ci0], csu1 = US[ci1], csv0 = VS[ci0], csv1 = VS[ci1];
;     ...
;     EXP_XROW(t0);
;     u32x4 A[EB], B[EB];
; #pragma unroll
;     for (int e = 0; e < EB; ++e) A[e] = EXP_ROW(ci0, e);
; #pragma unroll
;     for (int e = 0; e < EB; ++e) B[e] = EXP_ROW(ci0, EB + e);
.LBB0_1011:
	s_or_b64 exec, exec, s[12:13]
	s_waitcnt lgkmcnt(0)
	s_mul_i32 s8, s24, s96
	s_add_i32 s0, s8, s24
	s_min_i32 s17, s0, 0x8000
	s_sub_i32 s77, s96, s95
	s_add_i32 s77, s77, 8
	s_mul_i32 s77, s77, s24
	s_cmp_le_i32 s77, 0x8000
	s_cselect_b32 s77, 1, 0
	s_cmp_ge_i32 s8, s17
	s_waitcnt vmcnt(0)
	s_barrier
	s_cbranch_scc1 .LBB0_1025
	s_add_u32 s0, s6, 0xf800000
	s_addc_u32 s1, s7, 0
	s_add_u32 s10, s6, 0x1200000
	s_addc_u32 s11, s7, 0
	s_mov_b32 s80, s10
	s_and_b32 s81, s11, 0xffff
	s_mov_b32 s82, 0x1000000
	s_mov_b32 s83, 0x20000
	s_add_u32 s12, s6, 0x1100000
	s_addc_u32 s13, s7, 0
	s_add_u32 s14, s6, 0x1140000
	s_addc_u32 s15, s7, 0
	s_lshl_b32 s2, s95, 12
	s_add_i32 s26, s2, 0
	s_add_u32 s2, s6, 0x1b800000
	s_addc_u32 s3, s7, 0
	s_ashr_i32 s9, s8, 31
	s_lshl_b64 s[6:7], s[8:9], 9
	v_and_b32_e32 v74, 63, v0
	s_add_u32 s6, s0, s6
	s_addc_u32 s7, s1, s7
	v_lshlrev_b32_e32 v192, 2, v74
	global_load_dword v229, v192, s[6:7]
	global_load_dword v230, v192, s[6:7] offset:256
	s_lshl_b64 s[18:19], s[8:9], 11
	s_add_u32 s18, s2, s18
	s_addc_u32 s19, s3, s19
	s_lshl_b32 s9, s8, 11
	v_mov_b32_e32 v1, 0
	s_and_b32 s9, s9, 0x800
	v_lshlrev_b32_e32 v194, 4, v74
	v_mov_b32_e32 v195, v1
	s_add_i32 s9, s26, s9
	s_mov_b64 s[6:7], 0x400
	v_lshl_add_u64 v[2:3], s[18:19], 0, v[194:195]
	s_add_i32 m0, s9, 0x4000
	v_lshl_add_u64 v[2:3], v[2:3], 0, s[6:7]
	global_load_lds_dwordx4 v194, s[18:19] nt
	s_add_i32 m0, s9, 0x4400
	v_mov_b32_e32 v193, v1
	global_load_lds_dwordx4 v[2:3], off nt
	v_and_b32_e32 v77, 2, v0
	v_lshl_add_u64 v[196:197], s[0:1], 0, v[192:193]
	v_lshl_add_u64 v[198:199], s[2:3], 0, v[194:195]
	v_cmp_eq_u32_e64 s[0:1], 0, v77
	v_lshl_add_u64 v[200:201], s[4:5], 0, v[194:195]
	v_lshl_add_u32 v195, v74, 3, s26
	v_mov_b32_e32 v226, 0x358637bd
	v_mov_b32_e32 v227, 0xbf3a00e3
	s_waitcnt vmcnt(0)
	v_alignbit_b32 v229, v229, v229, 16
	v_alignbit_b32 v230, v230, v230, 16
	s_nop 1
	s_mov_b32 s58, 0x99999999
	s_mov_b32 s59, 0x99999999
	v_min_u32_dpp v202, v229, v229 quad_perm:[1,0,3,2] row_mask:0xf bank_mask:0xf
	v_max_u32_dpp v203, v229, v229 quad_perm:[1,0,3,2] row_mask:0xf bank_mask:0xf
	v_min_u32_dpp v204, v230, v230 quad_perm:[1,0,3,2] row_mask:0xf bank_mask:0xf
	v_max_u32_dpp v205, v230, v230 quad_perm:[1,0,3,2] row_mask:0xf bank_mask:0xf
	v_cndmask_b32_e64 v229, v203, v202, s[58:59]
	v_cndmask_b32_e64 v230, v205, v204, s[58:59]
	s_mov_b32 s58, 0xcc33cc33
	s_mov_b32 s59, 0xcc33cc33
	v_min_u32_dpp v202, v229, v229 quad_perm:[2,3,0,1] row_mask:0xf bank_mask:0xf
	v_max_u32_dpp v203, v229, v229 quad_perm:[2,3,0,1] row_mask:0xf bank_mask:0xf
	v_min_u32_dpp v204, v230, v230 quad_perm:[2,3,0,1] row_mask:0xf bank_mask:0xf
	v_max_u32_dpp v205, v230, v230 quad_perm:[2,3,0,1] row_mask:0xf bank_mask:0xf
	v_cndmask_b32_e64 v229, v203, v202, s[58:59]
	v_cndmask_b32_e64 v230, v205, v204, s[58:59]
	s_mov_b32 s58, 0xaa55aa55
	s_mov_b32 s59, 0xaa55aa55
	v_min_u32_dpp v202, v229, v229 quad_perm:[1,0,3,2] row_mask:0xf bank_mask:0xf
	v_max_u32_dpp v203, v229, v229 quad_perm:[1,0,3,2] row_mask:0xf bank_mask:0xf
	v_min_u32_dpp v204, v230, v230 quad_perm:[1,0,3,2] row_mask:0xf bank_mask:0xf
	v_max_u32_dpp v205, v230, v230 quad_perm:[1,0,3,2] row_mask:0xf bank_mask:0xf
	v_cndmask_b32_e64 v229, v203, v202, s[58:59]
	v_cndmask_b32_e64 v230, v205, v204, s[58:59]
	s_mov_b32 s58, 0xf00ff00f
	s_mov_b32 s59, 0xf00ff00f
	v_min_u32_dpp v202, v229, v229 row_ror:8 row_mask:0xf bank_mask:0xf
	v_max_u32_dpp v203, v229, v229 row_ror:8 row_mask:0xf bank_mask:0xf
	v_min_u32_dpp v204, v230, v230 row_ror:8 row_mask:0xf bank_mask:0xf
	v_max_u32_dpp v205, v230, v230 row_ror:8 row_mask:0xf bank_mask:0xf
	v_cndmask_b32_e64 v229, v203, v202, s[58:59]
	v_cndmask_b32_e64 v230, v205, v204, s[58:59]
	s_mov_b32 s58, 0xc3c3c3c3
	s_mov_b32 s59, 0xc3c3c3c3
	v_min_u32_dpp v202, v229, v229 quad_perm:[2,3,0,1] row_mask:0xf bank_mask:0xf
	v_max_u32_dpp v203, v229, v229 quad_perm:[2,3,0,1] row_mask:0xf bank_mask:0xf
	v_min_u32_dpp v204, v230, v230 quad_perm:[2,3,0,1] row_mask:0xf bank_mask:0xf
	v_max_u32_dpp v205, v230, v230 quad_perm:[2,3,0,1] row_mask:0xf bank_mask:0xf
	v_cndmask_b32_e64 v229, v203, v202, s[58:59]
	v_cndmask_b32_e64 v230, v205, v204, s[58:59]
	s_mov_b32 s58, 0xa5a5a5a5
	s_mov_b32 s59, 0xa5a5a5a5
	v_min_u32_dpp v202, v229, v229 quad_perm:[1,0,3,2] row_mask:0xf bank_mask:0xf
	v_max_u32_dpp v203, v229, v229 quad_perm:[1,0,3,2] row_mask:0xf bank_mask:0xf
	v_min_u32_dpp v204, v230, v230 quad_perm:[1,0,3,2] row_mask:0xf bank_mask:0xf
	v_max_u32_dpp v205, v230, v230 quad_perm:[1,0,3,2] row_mask:0xf bank_mask:0xf
	v_cndmask_b32_e64 v229, v203, v202, s[58:59]
	v_cndmask_b32_e64 v230, v205, v204, s[58:59]
	s_mov_b32 s58, 0xf0f00f0f
	s_mov_b32 s59, 0xf0f00f0f
	v_mov_b32_dpp v202, v229 row_half_mirror row_mask:0xf bank_mask:0xf
	v_mov_b32_dpp v204, v230 row_half_mirror row_mask:0xf bank_mask:0xf
	s_nop 0
	v_max_u32_dpp v203, v202, v229 quad_perm:[3,2,1,0] row_mask:0xf bank_mask:0xf
	v_max_u32_dpp v205, v204, v230 quad_perm:[3,2,1,0] row_mask:0xf bank_mask:0xf
	v_min_u32_dpp v202, v202, v229 quad_perm:[3,2,1,0] row_mask:0xf bank_mask:0xf
	v_min_u32_dpp v204, v204, v230 quad_perm:[3,2,1,0] row_mask:0xf bank_mask:0xf
	v_cndmask_b32_e64 v229, v203, v202, s[58:59]
	v_cndmask_b32_e64 v230, v205, v204, s[58:59]
	s_mov_b32 s58, 0xff0000ff
	s_mov_b32 s59, 0xff0000ff
	v_min_u32_dpp v202, v229, v229 row_ror:8 row_mask:0xf bank_mask:0xf
	v_max_u32_dpp v203, v229, v229 row_ror:8 row_mask:0xf bank_mask:0xf
	v_min_u32_dpp v204, v230, v230 row_ror:8 row_mask:0xf bank_mask:0xf
	v_max_u32_dpp v205, v230, v230 row_ror:8 row_mask:0xf bank_mask:0xf
	v_cndmask_b32_e64 v229, v203, v202, s[58:59]
; __device__ __forceinline__ void expert_tokens(const unsigned char* __restrict__ UV, const float* __restrict__ US, const float* __restrict__ VS, ...
;     ...
;     const unsigned cw0 = (unsigned)IDX[(size_t)t0 * 128 + lane], cw1 = (unsigned)IDX[(size_t)t0 * 128 + 64 + lane];
;     int ci0 = (int)cw0 & rmask, ci1 = (int)cw1 & rmask;
	v_cndmask_b32_e64 v230, v205, v204, s[58:59]
	s_mov_b32 s58, 0xcccc3333
	s_mov_b32 s59, 0xcccc3333
	v_min_u32_dpp v202, v229, v229 quad_perm:[2,3,0,1] row_mask:0xf bank_mask:0xf
	v_max_u32_dpp v203, v229, v229 quad_perm:[2,3,0,1] row_mask:0xf bank_mask:0xf
	v_min_u32_dpp v204, v230, v230 quad_perm:[2,3,0,1] row_mask:0xf bank_mask:0xf
	v_max_u32_dpp v205, v230, v230 quad_perm:[2,3,0,1] row_mask:0xf bank_mask:0xf
	v_cndmask_b32_e64 v229, v203, v202, s[58:59]
	v_cndmask_b32_e64 v230, v205, v204, s[58:59]
	s_mov_b32 s58, 0xaaaa5555
	s_mov_b32 s59, 0xaaaa5555
	v_min_u32_dpp v202, v229, v229 quad_perm:[1,0,3,2] row_mask:0xf bank_mask:0xf
	v_max_u32_dpp v203, v229, v229 quad_perm:[1,0,3,2] row_mask:0xf bank_mask:0xf
	v_min_u32_dpp v204, v230, v230 quad_perm:[1,0,3,2] row_mask:0xf bank_mask:0xf
	v_max_u32_dpp v205, v230, v230 quad_perm:[1,0,3,2] row_mask:0xf bank_mask:0xf
	v_cndmask_b32_e64 v229, v203, v202, s[58:59]
	v_cndmask_b32_e64 v230, v205, v204, s[58:59]
	s_nop 1
	v_permlane16_swap_b32_e32 v229, v230
	s_mov_b32 s58, -1
	s_mov_b32 s59, 0
	v_min_u32_e32 v202, v229, v230
	v_max_u32_e32 v203, v229, v230
	v_cndmask_b32_e64 v229, v203, v202, s[58:59]
	v_cndmask_b32_e64 v230, v202, v203, s[58:59]
	s_mov_b32 s58, 0xf0f0f0f
	s_mov_b32 s59, 0xf0f0f0f0
	v_mov_b32_dpp v202, v229 row_half_mirror row_mask:0xf bank_mask:0xf
	v_mov_b32_dpp v204, v230 row_half_mirror row_mask:0xf bank_mask:0xf
	s_nop 0
	v_max_u32_dpp v203, v202, v229 quad_perm:[3,2,1,0] row_mask:0xf bank_mask:0xf
	v_max_u32_dpp v205, v204, v230 quad_perm:[3,2,1,0] row_mask:0xf bank_mask:0xf
	v_min_u32_dpp v202, v202, v229 quad_perm:[3,2,1,0] row_mask:0xf bank_mask:0xf
	v_min_u32_dpp v204, v204, v230 quad_perm:[3,2,1,0] row_mask:0xf bank_mask:0xf
	v_cndmask_b32_e64 v229, v203, v202, s[58:59]
	v_cndmask_b32_e64 v230, v205, v204, s[58:59]
	s_mov_b32 s58, 0xff00ff
	s_mov_b32 s59, 0xff00ff00
	v_min_u32_dpp v202, v229, v229 row_ror:8 row_mask:0xf bank_mask:0xf
	v_max_u32_dpp v203, v229, v229 row_ror:8 row_mask:0xf bank_mask:0xf
	v_min_u32_dpp v204, v230, v230 row_ror:8 row_mask:0xf bank_mask:0xf
	v_max_u32_dpp v205, v230, v230 row_ror:8 row_mask:0xf bank_mask:0xf
	v_cndmask_b32_e64 v229, v203, v202, s[58:59]
	v_cndmask_b32_e64 v230, v205, v204, s[58:59]
	s_mov_b32 s58, 0x33333333
	s_mov_b32 s59, 0xcccccccc
	v_min_u32_dpp v202, v229, v229 quad_perm:[2,3,0,1] row_mask:0xf bank_mask:0xf
	v_max_u32_dpp v203, v229, v229 quad_perm:[2,3,0,1] row_mask:0xf bank_mask:0xf
	v_min_u32_dpp v204, v230, v230 quad_perm:[2,3,0,1] row_mask:0xf bank_mask:0xf
	v_max_u32_dpp v205, v230, v230 quad_perm:[2,3,0,1] row_mask:0xf bank_mask:0xf
	v_cndmask_b32_e64 v229, v203, v202, s[58:59]
	v_cndmask_b32_e64 v230, v205, v204, s[58:59]
	s_mov_b32 s58, 0x55555555
	s_mov_b32 s59, 0xaaaaaaaa
	v_min_u32_dpp v202, v229, v229 quad_perm:[1,0,3,2] row_mask:0xf bank_mask:0xf
	v_max_u32_dpp v203, v229, v229 quad_perm:[1,0,3,2] row_mask:0xf bank_mask:0xf
	v_min_u32_dpp v204, v230, v230 quad_perm:[1,0,3,2] row_mask:0xf bank_mask:0xf
	v_max_u32_dpp v205, v230, v230 quad_perm:[1,0,3,2] row_mask:0xf bank_mask:0xf
	v_cndmask_b32_e64 v229, v203, v202, s[58:59]
	v_cndmask_b32_e64 v230, v205, v204, s[58:59]
	s_nop 1
	v_permlane32_swap_b32_e32 v229, v230
	s_mov_b32 s58, 0xffff
	s_mov_b32 s59, 0xffff
	v_min_u32_e32 v202, v229, v230
	v_max_u32_e32 v203, v229, v230
	v_cndmask_b32_e64 v229, v203, v202, s[58:59]
	v_cndmask_b32_e64 v230, v202, v203, s[58:59]
	s_nop 1
	v_permlane32_swap_b32_e32 v229, v230
	s_mov_b32 s58, 0xffff
	s_mov_b32 s59, 0xffff
	v_min_u32_e32 v202, v229, v230
	v_max_u32_e32 v203, v229, v230
	v_cndmask_b32_e64 v229, v203, v202, s[58:59]
	v_cndmask_b32_e64 v230, v202, v203, s[58:59]
	s_mov_b32 s58, 0xf0f00f0f
	s_mov_b32 s59, 0xf0f00f0f
	v_mov_b32_dpp v202, v229 row_half_mirror row_mask:0xf bank_mask:0xf
	v_mov_b32_dpp v204, v230 row_half_mirror row_mask:0xf bank_mask:0xf
	s_nop 0
	v_max_u32_dpp v203, v202, v229 quad_perm:[3,2,1,0] row_mask:0xf bank_mask:0xf
	v_max_u32_dpp v205, v204, v230 quad_perm:[3,2,1,0] row_mask:0xf bank_mask:0xf
	v_min_u32_dpp v202, v202, v229 quad_perm:[3,2,1,0] row_mask:0xf bank_mask:0xf
	v_min_u32_dpp v204, v204, v230 quad_perm:[3,2,1,0] row_mask:0xf bank_mask:0xf
	v_cndmask_b32_e64 v229, v203, v202, s[58:59]
	v_cndmask_b32_e64 v230, v205, v204, s[58:59]
	s_mov_b32 s58, 0xff0000ff
	s_mov_b32 s59, 0xff0000ff
	v_min_u32_dpp v202, v229, v229 row_ror:8 row_mask:0xf bank_mask:0xf
	v_max_u32_dpp v203, v229, v229 row_ror:8 row_mask:0xf bank_mask:0xf
	v_min_u32_dpp v204, v230, v230 row_ror:8 row_mask:0xf bank_mask:0xf
	v_max_u32_dpp v205, v230, v230 row_ror:8 row_mask:0xf bank_mask:0xf
	v_cndmask_b32_e64 v229, v203, v202, s[58:59]
	v_cndmask_b32_e64 v230, v205, v204, s[58:59]
	s_mov_b32 s58, 0xcccc3333
	s_mov_b32 s59, 0xcccc3333
	v_min_u32_dpp v202, v229, v229 quad_perm:[2,3,0,1] row_mask:0xf bank_mask:0xf
	v_max_u32_dpp v203, v229, v229 quad_perm:[2,3,0,1] row_mask:0xf bank_mask:0xf
	v_min_u32_dpp v204, v230, v230 quad_perm:[2,3,0,1] row_mask:0xf bank_mask:0xf
	v_max_u32_dpp v205, v230, v230 quad_perm:[2,3,0,1] row_mask:0xf bank_mask:0xf
	v_cndmask_b32_e64 v229, v203, v202, s[58:59]
	v_cndmask_b32_e64 v230, v205, v204, s[58:59]
	s_mov_b32 s58, 0xaaaa5555
	s_mov_b32 s59, 0xaaaa5555
	v_min_u32_dpp v202, v229, v229 quad_perm:[1,0,3,2] row_mask:0xf bank_mask:0xf
	v_max_u32_dpp v203, v229, v229 quad_perm:[1,0,3,2] row_mask:0xf bank_mask:0xf
	v_min_u32_dpp v204, v230, v230 quad_perm:[1,0,3,2] row_mask:0xf bank_mask:0xf
	v_max_u32_dpp v205, v230, v230 quad_perm:[1,0,3,2] row_mask:0xf bank_mask:0xf
	v_cndmask_b32_e64 v229, v203, v202, s[58:59]
	v_cndmask_b32_e64 v230, v205, v204, s[58:59]
	s_nop 1
; #define EXP_ROW(src, l) (*(const u32x4*)(UV + ((unsigned)__builtin_amdgcn_readlane((src), (l)) * 1024u + lo16)))
; #define EXP_XROW(tt) do { const char* g_ = (const char*)(xin + (size_t)(tt) * 1024) + lane * 16; LAS unsigned char* l_ = xslot + ((tt) & 1) * 2048; \
;         __builtin_amdgcn_global_load_lds((const unsigned*)g_, (LAS unsigned*)l_, 16, 0, 2); __builtin_amdgcn_global_load_lds((const unsigned*)(g_ + 1024), (LAS unsigned*)(l_ + 1024), 16, 0, 2); } while (0)
; __device__ __forceinline__ void expert_tokens(const unsigned char* __restrict__ UV, const float* __restrict__ US, const float* __restrict__ VS, ...
;     ...
;     const unsigned cw0 = (unsigned)IDX[(size_t)t0 * 128 + lane], cw1 = (unsigned)IDX[(size_t)t0 * 128 + 64 + lane];
;     int ci0 = (int)cw0 & rmask, ci1 = (int)cw1 & rmask;
;     float cg0 = __uint_as_float(cw0 & 0xFFFF0000u), cg1 = __uint_as_float(cw1 & 0xFFFF0000u);
;     float csu0 = US[ci0], csu1 = US[ci1], csv0 = VS[ci0], csv1 = VS[ci1];
;     ...
;     EXP_XROW(t0);
;     u32x4 A[EB], B[EB];
; #pragma unroll
;     for (int e = 0; e < EB; ++e) A[e] = EXP_ROW(ci0, e);
; #pragma unroll
;     for (int e = 0; e < EB; ++e) B[e] = EXP_ROW(ci0, EB + e);
	v_permlane16_swap_b32_e32 v229, v230
	v_min_u32_e32 v202, v229, v230
	v_max_u32_e32 v230, v229, v230
	v_mov_b32_e32 v229, v202
	s_nop 1
	v_permlane32_swap_b32_e32 v229, v230
	v_min_u32_e32 v202, v229, v230
	v_max_u32_e32 v230, v229, v230
	v_mov_b32_e32 v229, v202
	s_nop 1
	v_permlane16_swap_b32_e32 v229, v230
	v_min_u32_e32 v202, v229, v230
	v_max_u32_e32 v230, v229, v230
	v_mov_b32_e32 v229, v202
	s_mov_b32 s58, 0xf0f0f0f
	s_mov_b32 s59, 0xf0f0f0f
	v_mov_b32_dpp v202, v229 row_half_mirror row_mask:0xf bank_mask:0xf
	v_mov_b32_dpp v204, v230 row_half_mirror row_mask:0xf bank_mask:0xf
	s_nop 0
	v_max_u32_dpp v203, v202, v229 quad_perm:[3,2,1,0] row_mask:0xf bank_mask:0xf
	v_max_u32_dpp v205, v204, v230 quad_perm:[3,2,1,0] row_mask:0xf bank_mask:0xf
	v_min_u32_dpp v202, v202, v229 quad_perm:[3,2,1,0] row_mask:0xf bank_mask:0xf
	v_min_u32_dpp v204, v204, v230 quad_perm:[3,2,1,0] row_mask:0xf bank_mask:0xf
	v_cndmask_b32_e64 v229, v203, v202, s[58:59]
	v_cndmask_b32_e64 v230, v205, v204, s[58:59]
	s_mov_b32 s58, 0xff00ff
	s_mov_b32 s59, 0xff00ff
	v_min_u32_dpp v202, v229, v229 row_ror:8 row_mask:0xf bank_mask:0xf
	v_max_u32_dpp v203, v229, v229 row_ror:8 row_mask:0xf bank_mask:0xf
	v_min_u32_dpp v204, v230, v230 row_ror:8 row_mask:0xf bank_mask:0xf
	v_max_u32_dpp v205, v230, v230 row_ror:8 row_mask:0xf bank_mask:0xf
	v_cndmask_b32_e64 v229, v203, v202, s[58:59]
	v_cndmask_b32_e64 v230, v205, v204, s[58:59]
	s_mov_b32 s58, 0x33333333
	s_mov_b32 s59, 0x33333333
	v_min_u32_dpp v202, v229, v229 quad_perm:[2,3,0,1] row_mask:0xf bank_mask:0xf
	v_max_u32_dpp v203, v229, v229 quad_perm:[2,3,0,1] row_mask:0xf bank_mask:0xf
	v_min_u32_dpp v204, v230, v230 quad_perm:[2,3,0,1] row_mask:0xf bank_mask:0xf
	v_max_u32_dpp v205, v230, v230 quad_perm:[2,3,0,1] row_mask:0xf bank_mask:0xf
	v_cndmask_b32_e64 v229, v203, v202, s[58:59]
	v_cndmask_b32_e64 v230, v205, v204, s[58:59]
	s_mov_b32 s58, 0x55555555
	s_mov_b32 s59, 0x55555555
	v_min_u32_dpp v202, v229, v229 quad_perm:[1,0,3,2] row_mask:0xf bank_mask:0xf
	v_max_u32_dpp v203, v229, v229 quad_perm:[1,0,3,2] row_mask:0xf bank_mask:0xf
	v_min_u32_dpp v204, v230, v230 quad_perm:[1,0,3,2] row_mask:0xf bank_mask:0xf
	v_max_u32_dpp v205, v230, v230 quad_perm:[1,0,3,2] row_mask:0xf bank_mask:0xf
	v_cndmask_b32_e64 v229, v203, v202, s[58:59]
	v_cndmask_b32_e64 v230, v205, v204, s[58:59]
	s_nop 1
	v_permlane16_swap_b32_e32 v229, v230
	s_nop 1
	v_permlane32_swap_b32_e32 v229, v230
	v_alignbit_b32 v229, v229, v229, 16
	v_alignbit_b32 v230, v230, v230, 16
	v_and_b32_e32 v231, 0x3fff, v229
	v_and_b32_e32 v232, 0x3fff, v230
	v_readlane_b32 s40, v231, 22
	v_readlane_b32 s41, v231, 23
	v_readlane_b32 s49, v231, 31
	v_lshlrev_b32_e32 v2, 2, v231
	v_lshlrev_b32_e32 v3, 2, v232
	v_readlane_b32 s33, v231, 15
	v_readlane_b32 s34, v231, 16
	v_readlane_b32 s35, v231, 17
	v_readlane_b32 s36, v231, 18
	v_readlane_b32 s37, v231, 19
	v_readlane_b32 s38, v231, 20
	v_readlane_b32 s39, v231, 21
	v_readlane_b32 s42, v231, 24
	v_readlane_b32 s43, v231, 25
	v_readlane_b32 s44, v231, 26
	v_readlane_b32 s45, v231, 27
	v_readlane_b32 s46, v231, 28
	v_readlane_b32 s47, v231, 29
	v_readlane_b32 s48, v231, 30
	v_lshl_or_b32 v42, s49, 10, v194
	v_lshl_or_b32 v50, s41, 10, v194
	v_lshl_or_b32 v51, s40, 10, v194
	v_readlane_b32 s30, v231, 13
	v_readlane_b32 s31, v231, 14
	global_load_dword v233, v2, s[12:13]
	global_load_dword v234, v3, s[12:13]
	global_load_dword v236, v3, s[14:15]
	global_load_dword v235, v2, s[14:15]
	v_lshl_or_b32 v43, s48, 10, v194
	v_lshl_or_b32 v44, s47, 10, v194
	v_lshl_or_b32 v45, s46, 10, v194
	v_lshl_or_b32 v46, s45, 10, v194
	v_lshl_or_b32 v47, s44, 10, v194
	v_lshl_or_b32 v48, s43, 10, v194
	v_lshl_or_b32 v49, s42, 10, v194
	global_load_dwordx4 v[2:5], v42, s[10:11]
	global_load_dwordx4 v[10:13], v43, s[10:11]
	global_load_dwordx4 v[6:9], v44, s[10:11]
	global_load_dwordx4 v[18:21], v45, s[10:11]
	global_load_dwordx4 v[14:17], v46, s[10:11]
	global_load_dwordx4 v[26:29], v47, s[10:11]
	global_load_dwordx4 v[22:25], v48, s[10:11]
	global_load_dwordx4 v[34:37], v49, s[10:11]
	global_load_dwordx4 v[30:33], v50, s[10:11]
	global_load_dwordx4 v[38:41], v51, s[10:11]
	v_lshl_or_b32 v50, s39, 10, v194
	v_lshl_or_b32 v51, s38, 10, v194
	v_lshl_or_b32 v58, s37, 10, v194
	v_lshl_or_b32 v59, s36, 10, v194
	v_lshl_or_b32 v66, s35, 10, v194
	v_lshl_or_b32 v67, s34, 10, v194
	v_lshl_or_b32 v75, s33, 10, v194
	v_readlane_b32 s28, v231, 11
	v_readlane_b32 s29, v231, 12
	global_load_dwordx4 v[42:45], v50, s[10:11]
	global_load_dwordx4 v[46:49], v51, s[10:11]
	s_nop 0
	global_load_dwordx4 v[50:53], v58, s[10:11]
	global_load_dwordx4 v[54:57], v59, s[10:11]
	s_nop 0
	global_load_dwordx4 v[58:61], v66, s[10:11]
	global_load_dwordx4 v[62:65], v67, s[10:11]
	v_lshl_or_b32 v76, s31, 10, v194
	global_load_dwordx4 v[66:69], v75, s[10:11]
	global_load_dwordx4 v[70:73], v76, s[10:11]
	v_lshl_or_b32 v75, s30, 10, v194
	v_readlane_b32 s25, v231, 9
	v_readlane_b32 s27, v231, 10
	v_lshl_or_b32 v76, s29, 10, v194
	global_load_dwordx4 v[112:115], v75, s[10:11]
	global_load_dwordx4 v[116:119], v76, s[10:11]
	v_lshl_or_b32 v75, s28, 10, v194
	v_readlane_b32 s23, v231, 7
	v_readlane_b32 s24, v231, 8
	v_lshl_or_b32 v76, s27, 10, v194
	global_load_dwordx4 v[144:147], v75, s[10:11]
	global_load_dwordx4 v[148:151], v76, s[10:11]
	v_lshl_or_b32 v75, s25, 10, v194
	v_readlane_b32 s21, v231, 5
	v_readlane_b32 s22, v231, 6
	v_lshl_or_b32 v76, s24, 10, v194
	global_load_dwordx4 v[152:155], v75, s[10:11]
	global_load_dwordx4 v[156:159], v76, s[10:11]
	v_lshl_or_b32 v75, s23, 10, v194
	v_readlane_b32 s19, v231, 3
	v_readlane_b32 s20, v231, 4
	v_lshl_or_b32 v76, s22, 10, v194
	global_load_dwordx4 v[160:163], v75, s[10:11]
	global_load_dwordx4 v[164:167], v76, s[10:11]
	v_lshl_or_b32 v75, s21, 10, v194
	v_readlane_b32 s16, v231, 1
	v_readlane_b32 s18, v231, 2
	v_lshl_or_b32 v76, s20, 10, v194
	global_load_dwordx4 v[168:171], v75, s[10:11]
	global_load_dwordx4 v[172:175], v76, s[10:11]
	v_lshl_or_b32 v75, s19, 10, v194
	v_readlane_b32 s9, v231, 0
	v_lshl_or_b32 v76, s18, 10, v194
	global_load_dwordx4 v[176:179], v75, s[10:11]
	global_load_dwordx4 v[180:183], v76, s[10:11]
	v_lshl_or_b32 v75, s16, 10, v194
	v_lshl_or_b32 v76, s9, 10, v194
	global_load_dwordx4 v[184:187], v75, s[10:11]
	global_load_dwordx4 v[188:191], v76, s[10:11]
	v_and_b32_e32 v75, 1, v0
	v_lshrrev_b32_e32 v76, 2, v0
	v_and_b32_e32 v0, 3, v0
	v_and_or_b32 v193, v76, 12, v0
	v_cmp_eq_u32_e64 s[2:3], 0, v75
	v_mbcnt_lo_u32_b32 v0, -1, 0
	s_mov_b32 s9, 0x800000
	s_mov_b32 s16, 0x45800000
	s_mov_b32 s27, 0x42ee0000
	s_mov_b32 s28, 0x3e6d3388
	s_mov_b32 s29, 0xc040c00
	s_mov_b32 s30, 0xc050c01
	s_mov_b32 s31, 0xc060c02
	s_mov_b32 s33, 0xc070c03
	v_mbcnt_hi_u32_b32 v228, -1, v0
	s_mov_b32 s20, s8
	s_branch .LBB0_1014

.Lp10_nobar_i:
	v_dot8_i32_i4 v88, v248, v70, 0
	v_dot8_i32_i4 v88, v250, v71, v88
	s_nop 2
	v_lshlrev_b32_e32 v88, 4, v88
	v_dot8_i32_i4 v88, v247, v70, v88
	v_dot8_i32_i4 v74, v248, v188, 0
	v_dot8_i32_i4 v75, v248, v184, 0
	v_dot8_i32_i4 v76, v248, v180, 0
	v_dot8_i32_i4 v77, v248, v176, 0
	v_dot8_i32_i4 v78, v248, v172, 0
	v_dot8_i32_i4 v79, v248, v168, 0
	v_dot8_i32_i4 v80, v248, v164, 0
	v_dot8_i32_i4 v81, v248, v160, 0
	v_dot8_i32_i4 v82, v248, v156, 0
	v_dot8_i32_i4 v83, v248, v152, 0
	v_dot8_i32_i4 v84, v248, v148, 0
	v_dot8_i32_i4 v85, v248, v144, 0
	v_dot8_i32_i4 v86, v248, v116, 0
	v_dot8_i32_i4 v87, v248, v112, 0
	v_dot8_i32_i4 v70, v248, v66, 0
	v_dot8_i32_i4 v74, v250, v189, v74
	v_dot8_i32_i4 v75, v250, v185, v75
	v_dot8_i32_i4 v76, v250, v181, v76
	v_dot8_i32_i4 v77, v250, v177, v77
	v_dot8_i32_i4 v78, v250, v173, v78
	v_dot8_i32_i4 v79, v250, v169, v79
	v_dot8_i32_i4 v80, v250, v165, v80
	v_dot8_i32_i4 v81, v250, v161, v81
	v_dot8_i32_i4 v82, v250, v157, v82
	v_dot8_i32_i4 v83, v250, v153, v83
	v_dot8_i32_i4 v84, v250, v149, v84
	v_dot8_i32_i4 v85, v250, v145, v85
	v_dot8_i32_i4 v86, v250, v117, v86
	v_dot8_i32_i4 v87, v250, v113, v87
	v_dot8_i32_i4 v70, v250, v67, v70
	v_lshlrev_b32_e32 v74, 4, v74
	v_lshlrev_b32_e32 v75, 4, v75
	v_lshlrev_b32_e32 v76, 4, v76
	v_lshlrev_b32_e32 v77, 4, v77
	v_lshlrev_b32_e32 v78, 4, v78
	v_lshlrev_b32_e32 v79, 4, v79
	v_lshlrev_b32_e32 v80, 4, v80
	v_lshlrev_b32_e32 v81, 4, v81
	v_lshlrev_b32_e32 v82, 4, v82
	v_lshlrev_b32_e32 v83, 4, v83
	v_lshlrev_b32_e32 v84, 4, v84
	v_lshlrev_b32_e32 v85, 4, v85
	v_lshlrev_b32_e32 v86, 4, v86
	v_lshlrev_b32_e32 v87, 4, v87
	v_lshlrev_b32_e32 v70, 4, v70
	v_dot8_i32_i4 v74, v247, v188, v74
	v_dot8_i32_i4 v75, v247, v184, v75
	v_dot8_i32_i4 v76, v247, v180, v76
	v_dot8_i32_i4 v77, v247, v176, v77
	v_dot8_i32_i4 v78, v247, v172, v78
	v_dot8_i32_i4 v79, v247, v168, v79
	v_dot8_i32_i4 v80, v247, v164, v80
	v_dot8_i32_i4 v81, v247, v160, v81
	v_dot8_i32_i4 v82, v247, v156, v82
	v_dot8_i32_i4 v83, v247, v152, v83
	v_dot8_i32_i4 v84, v247, v148, v84
	v_dot8_i32_i4 v85, v247, v144, v85
	v_dot8_i32_i4 v86, v247, v116, v86
	v_dot8_i32_i4 v87, v247, v112, v87
	v_dot8_i32_i4 v70, v247, v66, v70
	v_dot8_i32_i4 v74, v249, v189, v74
	v_dot8_i32_i4 v75, v249, v185, v75
	v_dot8_i32_i4 v76, v249, v181, v76
	v_dot8_i32_i4 v77, v249, v177, v77
	v_dot8_i32_i4 v78, v249, v173, v78
	v_dot8_i32_i4 v79, v249, v169, v79
	v_dot8_i32_i4 v80, v249, v165, v80
	v_dot8_i32_i4 v81, v249, v161, v81
	v_dot8_i32_i4 v82, v249, v157, v82
	v_dot8_i32_i4 v83, v249, v153, v83
	v_dot8_i32_i4 v84, v249, v149, v84
	v_dot8_i32_i4 v85, v249, v145, v85
	v_dot8_i32_i4 v86, v249, v117, v86
	v_dot8_i32_i4 v87, v249, v113, v87
	v_dot8_i32_i4 v88, v249, v71, v88
	v_dot8_i32_i4 v70, v249, v67, v70
	v_permlane32_swap_b32_e32 v74, v82
	v_permlane32_swap_b32_e32 v75, v83
	v_permlane32_swap_b32_e32 v76, v84
	v_permlane32_swap_b32_e32 v77, v85
	v_permlane32_swap_b32_e32 v78, v86
	v_permlane32_swap_b32_e32 v79, v87
	v_permlane32_swap_b32_e32 v80, v88
	v_permlane32_swap_b32_e32 v81, v70
	v_add_u32_e32 v66, v74, v82
	v_add_u32_e32 v67, v75, v83
	v_add_u32_e32 v71, v76, v84
	v_add_u32_e32 v74, v77, v85
	v_add_u32_e32 v75, v78, v86
	v_add_u32_e32 v76, v79, v87
	v_add_u32_e32 v77, v80, v88
	v_add_u32_e32 v70, v81, v70
	v_permlane16_swap_b32_e32 v66, v75
	v_permlane16_swap_b32_e32 v67, v76
	v_permlane16_swap_b32_e32 v71, v77
	v_permlane16_swap_b32_e32 v74, v70
	v_add_u32_e32 v66, v66, v75
	v_add_u32_e32 v67, v67, v76
	v_add_u32_e32 v71, v71, v77
	v_add_u32_e32 v70, v74, v70
	v_cndmask_b32_e64 v74, v71, v66, s[0:1]
	v_cndmask_b32_e64 v66, v66, v71, s[0:1]
	v_cndmask_b32_e64 v71, v70, v67, s[0:1]
	v_cndmask_b32_e64 v67, v67, v70, s[0:1]
	v_add_u32_dpp v66, v66, v74 quad_perm:[2,3,0,1] row_mask:0xf bank_mask:0xf bound_ctrl:1
	s_sub_i32 s4, s21, 32
	v_add_u32_dpp v67, v67, v71 quad_perm:[2,3,0,1] row_mask:0xf bank_mask:0xf bound_ctrl:1
	v_cndmask_b32_e64 v70, v67, v66, s[2:3]
	v_cndmask_b32_e64 v66, v66, v67, s[2:3]
	s_cmp_lt_u32 s25, 4
	s_cselect_b64 vcc, -1, 0
	v_add_u32_dpp v66, v66, v70 quad_perm:[1,0,3,2] row_mask:0xf bank_mask:0xf bound_ctrl:1
	v_cndmask_b32_e32 v70, v234, v233, vcc
	v_cndmask_b32_e32 v71, v230, v229, vcc
	v_add_u32_dpp v66, v66, v66 row_ror:8 row_mask:0xf bank_mask:0xf bound_ctrl:1
	s_cmp_eq_u32 s21, 32
	s_nop 0
	v_add_u32_dpp v67, v66, v66 row_ror:4 row_mask:0xf bank_mask:0xf bound_ctrl:1
	v_and_or_b32 v66, s4, 32, v193
	v_lshlrev_b32_e32 v66, 2, v66
	v_cvt_f32_i32_e32 v74, v67
	ds_bpermute_b32 v75, v66, v70
	v_and_b32_e32 v67, 0xffff0000, v71
	ds_bpermute_b32 v76, v66, v67
	v_add_f32_e32 v71, v251, v74
	v_mul_f32_e32 v71, v244, v71
	s_waitcnt lgkmcnt(1)
	v_mul_f32_e32 v74, v71, v75
	v_fma_f32 v71, |v74|, s28, 1.0
	v_rcp_f32_e32 v75, v71
	v_mul_f32_e32 v79, v74, v74
	v_mul_f32_e32 v79, 0xbf38aa3b, v79
	v_exp_f32_e32 v79, v79
	v_fmamk_f32 v78, v75, 0x3f07dc22, v227
	v_fmaak_f32 v78, v75, v78, 0x3f35f0e3
	v_fmaak_f32 v78, v75, v78, 0xbe11a98e
	v_cndmask_b32_e32 v71, v236, v235, vcc
	v_fmaak_f32 v78, v75, v78, 0x3e027906
	ds_bpermute_b32 v77, v66, v71
	v_mul_f32_e32 v75, v75, v78
	v_mul_f32_e32 v75, v79, v75
	v_mul_f32_e32 v78, v74, v75
	v_fma_f32 v75, -v74, v75, v74
	v_cmp_gt_f32_e32 vcc, 0, v74
	s_nop 1
	v_cndmask_b32_e32 v74, v75, v78, vcc
	s_waitcnt lgkmcnt(1)
	v_mul_f32_e32 v74, v74, v76
	s_cselect_b64 vcc, -1, 0
	s_cmp_gt_u32 s25, 5
	s_waitcnt lgkmcnt(0)
; __device__ __forceinline__ void expert_tokens(const unsigned char* __restrict__ UV, const float* __restrict__ US, const float* __restrict__ VS, ...
;     ...
;         const unsigned nw0 = (unsigned)IDX[(size_t)tn * 128 + lane], nw1 = (unsigned)IDX[(size_t)tn * 128 + 64 + lane];
;         const int ni0 = (int)nw0 & rmask, ni1 = (int)nw1 & rmask;
;         const float ng0 = __uint_as_float(nw0 & 0xFFFF0000u), ng1 = __uint_as_float(nw1 & 0xFFFF0000u);
	v_mul_f32_e32 v74, v74, v77
	s_cselect_b64 s[22:23], -1, 0
	s_cmp_lt_u32 s25, 6
	v_fma_mixlo_f16 v116, v74, s16, 0
	s_cselect_b64 s[4:5], -1, 0
	v_and_b32_e32 v117, 0xffff, v116
	v_cndmask_b32_e64 v74, v242, v232, s[4:5]
	s_add_i32 s24, s21, 1
	s_add_i32 s35, s21, 2
	s_add_i32 s36, s21, 3
	s_add_i32 s37, s21, 4
	s_add_i32 s38, s21, 5
	s_add_i32 s39, s21, 6
	s_add_i32 s40, s21, 7
	s_add_i32 s49, s21, 8
	s_add_i32 s50, s21, 9
	s_add_i32 s51, s21, 10
	s_add_i32 s52, s21, 11
	s_add_i32 s53, s21, 12
	s_add_i32 s54, s21, 13
	s_add_i32 s55, s21, 14
	s_add_i32 s56, s21, 15
	v_cndmask_b32_e32 v136, v74, v231, vcc
	v_mov_b32_dpp v207, v117 quad_perm:[1,0,3,2] row_mask:0xf bank_mask:0xf
	v_lshlrev_b32_e32 v136, 10, v136
	s_cmp_lg_u32 s21, 32
	v_readlane_b32 s61, v136, s21
	v_readlane_b32 s62, v136, s24
	v_readlane_b32 s63, v136, s35
	v_readlane_b32 s64, v136, s36
	v_readlane_b32 s65, v136, s37
	v_readlane_b32 s66, v136, s38
	v_readlane_b32 s67, v136, s39
	v_readlane_b32 s68, v136, s40
	v_readlane_b32 s69, v136, s49
	v_readlane_b32 s70, v136, s50
	v_readlane_b32 s71, v136, s51
	v_readlane_b32 s72, v136, s52
	v_readlane_b32 s73, v136, s53
	v_readlane_b32 s74, v136, s54
	v_readlane_b32 s75, v136, s55
	v_readlane_b32 s76, v136, s56
	v_lshl_or_b32 v209, v207, 16, v117
	s_nop 0
	v_readlane_b32 s47, v209, 0
	v_readlane_b32 s45, v209, 2
	v_readlane_b32 s43, v209, 16
	v_readlane_b32 s41, v209, 18
	v_readlane_b32 s39, v209, 32
	v_readlane_b32 s37, v209, 34
	v_readlane_b32 s35, v209, 48
	v_readlane_b32 s4, v209, 50
	buffer_load_dwordx4 v[78:81], v194, s[80:83], s61 offen
	buffer_load_dwordx4 v[74:77], v194, s[80:83], s62 offen
	buffer_load_dwordx4 v[86:89], v194, s[80:83], s63 offen
	buffer_load_dwordx4 v[82:85], v194, s[80:83], s64 offen
	buffer_load_dwordx4 v[94:97], v194, s[80:83], s65 offen
	buffer_load_dwordx4 v[90:93], v194, s[80:83], s66 offen
	buffer_load_dwordx4 v[102:105], v194, s[80:83], s67 offen
	buffer_load_dwordx4 v[98:101], v194, s[80:83], s68 offen
	buffer_load_dwordx4 v[110:113], v194, s[80:83], s69 offen
	buffer_load_dwordx4 v[106:109], v194, s[80:83], s70 offen
	buffer_load_dwordx4 v[124:127], v194, s[80:83], s71 offen
	buffer_load_dwordx4 v[120:123], v194, s[80:83], s72 offen
	buffer_load_dwordx4 v[132:135], v194, s[80:83], s73 offen
	buffer_load_dwordx4 v[128:131], v194, s[80:83], s74 offen
	buffer_load_dwordx4 v[140:143], v194, s[80:83], s75 offen
	buffer_load_dwordx4 v[136:139], v194, s[80:83], s76 offen
	s_cbranch_scc1 .LBB0_1021
	s_waitcnt vmcnt(16)
	s_bfe_i32 s60, s34, 0x10000
	v_alignbit_b32 v237, v237, v237, 16
	v_alignbit_b32 v238, v238, v238, 16
	v_xor_b32_e32 v237, s60, v237
	v_xor_b32_e32 v238, s60, v238
	s_nop 1
	s_mov_b32 s58, 0x99999999
	s_mov_b32 s59, 0x99999999
	v_min_u32_dpp v202, v237, v237 quad_perm:[1,0,3,2] row_mask:0xf bank_mask:0xf
	v_max_u32_dpp v203, v237, v237 quad_perm:[1,0,3,2] row_mask:0xf bank_mask:0xf
	v_min_u32_dpp v204, v238, v238 quad_perm:[1,0,3,2] row_mask:0xf bank_mask:0xf
	v_max_u32_dpp v205, v238, v238 quad_perm:[1,0,3,2] row_mask:0xf bank_mask:0xf
	v_cndmask_b32_e64 v237, v203, v202, s[58:59]
	v_cndmask_b32_e64 v238, v205, v204, s[58:59]
	s_mov_b32 s58, 0xcc33cc33
	s_mov_b32 s59, 0xcc33cc33
	v_min_u32_dpp v202, v237, v237 quad_perm:[2,3,0,1] row_mask:0xf bank_mask:0xf
	v_max_u32_dpp v203, v237, v237 quad_perm:[2,3,0,1] row_mask:0xf bank_mask:0xf
	v_min_u32_dpp v204, v238, v238 quad_perm:[2,3,0,1] row_mask:0xf bank_mask:0xf
	v_max_u32_dpp v205, v238, v238 quad_perm:[2,3,0,1] row_mask:0xf bank_mask:0xf
	v_cndmask_b32_e64 v237, v203, v202, s[58:59]
	v_cndmask_b32_e64 v238, v205, v204, s[58:59]
	s_mov_b32 s58, 0xaa55aa55
	s_mov_b32 s59, 0xaa55aa55
	v_min_u32_dpp v202, v237, v237 quad_perm:[1,0,3,2] row_mask:0xf bank_mask:0xf
	v_max_u32_dpp v203, v237, v237 quad_perm:[1,0,3,2] row_mask:0xf bank_mask:0xf
	v_min_u32_dpp v204, v238, v238 quad_perm:[1,0,3,2] row_mask:0xf bank_mask:0xf
	v_max_u32_dpp v205, v238, v238 quad_perm:[1,0,3,2] row_mask:0xf bank_mask:0xf
	v_cndmask_b32_e64 v237, v203, v202, s[58:59]
	v_cndmask_b32_e64 v238, v205, v204, s[58:59]
	s_mov_b32 s58, 0xf00ff00f
	s_mov_b32 s59, 0xf00ff00f
	v_min_u32_dpp v202, v237, v237 row_ror:8 row_mask:0xf bank_mask:0xf
	v_max_u32_dpp v203, v237, v237 row_ror:8 row_mask:0xf bank_mask:0xf
	v_min_u32_dpp v204, v238, v238 row_ror:8 row_mask:0xf bank_mask:0xf
	v_max_u32_dpp v205, v238, v238 row_ror:8 row_mask:0xf bank_mask:0xf
	v_cndmask_b32_e64 v237, v203, v202, s[58:59]
	v_cndmask_b32_e64 v238, v205, v204, s[58:59]
	s_mov_b32 s58, 0xc3c3c3c3
	s_mov_b32 s59, 0xc3c3c3c3
	v_min_u32_dpp v202, v237, v237 quad_perm:[2,3,0,1] row_mask:0xf bank_mask:0xf
	v_max_u32_dpp v203, v237, v237 quad_perm:[2,3,0,1] row_mask:0xf bank_mask:0xf
	v_min_u32_dpp v204, v238, v238 quad_perm:[2,3,0,1] row_mask:0xf bank_mask:0xf
	v_max_u32_dpp v205, v238, v238 quad_perm:[2,3,0,1] row_mask:0xf bank_mask:0xf
	v_cndmask_b32_e64 v237, v203, v202, s[58:59]
	v_cndmask_b32_e64 v238, v205, v204, s[58:59]
	s_mov_b32 s58, 0xa5a5a5a5
	s_mov_b32 s59, 0xa5a5a5a5
	v_min_u32_dpp v202, v237, v237 quad_perm:[1,0,3,2] row_mask:0xf bank_mask:0xf
	v_max_u32_dpp v203, v237, v237 quad_perm:[1,0,3,2] row_mask:0xf bank_mask:0xf
	v_min_u32_dpp v204, v238, v238 quad_perm:[1,0,3,2] row_mask:0xf bank_mask:0xf
	v_max_u32_dpp v205, v238, v238 quad_perm:[1,0,3,2] row_mask:0xf bank_mask:0xf
	v_cndmask_b32_e64 v237, v203, v202, s[58:59]
	v_cndmask_b32_e64 v238, v205, v204, s[58:59]
	s_mov_b32 s58, 0xf0f00f0f
	s_mov_b32 s59, 0xf0f00f0f
	v_mov_b32_dpp v202, v237 row_half_mirror row_mask:0xf bank_mask:0xf
	v_mov_b32_dpp v204, v238 row_half_mirror row_mask:0xf bank_mask:0xf
	s_nop 0
; __device__ __forceinline__ void expert_tokens(const unsigned char* __restrict__ UV, const float* __restrict__ US, const float* __restrict__ VS, ...
;     ...
;         const unsigned nw0 = (unsigned)IDX[(size_t)tn * 128 + lane], nw1 = (unsigned)IDX[(size_t)tn * 128 + 64 + lane];
;         const int ni0 = (int)nw0 & rmask, ni1 = (int)nw1 & rmask;
;         const float ng0 = __uint_as_float(nw0 & 0xFFFF0000u), ng1 = __uint_as_float(nw1 & 0xFFFF0000u);
	v_max_u32_dpp v203, v202, v237 quad_perm:[3,2,1,0] row_mask:0xf bank_mask:0xf
	v_max_u32_dpp v205, v204, v238 quad_perm:[3,2,1,0] row_mask:0xf bank_mask:0xf
	v_min_u32_dpp v202, v202, v237 quad_perm:[3,2,1,0] row_mask:0xf bank_mask:0xf
	v_min_u32_dpp v204, v204, v238 quad_perm:[3,2,1,0] row_mask:0xf bank_mask:0xf
	v_cndmask_b32_e64 v237, v203, v202, s[58:59]
	v_cndmask_b32_e64 v238, v205, v204, s[58:59]
	s_mov_b32 s58, 0xff0000ff
	s_mov_b32 s59, 0xff0000ff
	v_min_u32_dpp v202, v237, v237 row_ror:8 row_mask:0xf bank_mask:0xf
	v_max_u32_dpp v203, v237, v237 row_ror:8 row_mask:0xf bank_mask:0xf
	v_min_u32_dpp v204, v238, v238 row_ror:8 row_mask:0xf bank_mask:0xf
	v_max_u32_dpp v205, v238, v238 row_ror:8 row_mask:0xf bank_mask:0xf
	v_cndmask_b32_e64 v237, v203, v202, s[58:59]
	v_cndmask_b32_e64 v238, v205, v204, s[58:59]
	s_mov_b32 s58, 0xcccc3333
	s_mov_b32 s59, 0xcccc3333
	v_min_u32_dpp v202, v237, v237 quad_perm:[2,3,0,1] row_mask:0xf bank_mask:0xf
	v_max_u32_dpp v203, v237, v237 quad_perm:[2,3,0,1] row_mask:0xf bank_mask:0xf
	v_min_u32_dpp v204, v238, v238 quad_perm:[2,3,0,1] row_mask:0xf bank_mask:0xf
	v_max_u32_dpp v205, v238, v238 quad_perm:[2,3,0,1] row_mask:0xf bank_mask:0xf
	v_cndmask_b32_e64 v237, v203, v202, s[58:59]
	v_cndmask_b32_e64 v238, v205, v204, s[58:59]
	s_mov_b32 s58, 0xaaaa5555
	s_mov_b32 s59, 0xaaaa5555
	v_min_u32_dpp v202, v237, v237 quad_perm:[1,0,3,2] row_mask:0xf bank_mask:0xf
	v_max_u32_dpp v203, v237, v237 quad_perm:[1,0,3,2] row_mask:0xf bank_mask:0xf
	v_min_u32_dpp v204, v238, v238 quad_perm:[1,0,3,2] row_mask:0xf bank_mask:0xf
	v_max_u32_dpp v205, v238, v238 quad_perm:[1,0,3,2] row_mask:0xf bank_mask:0xf
	v_cndmask_b32_e64 v237, v203, v202, s[58:59]
	v_cndmask_b32_e64 v238, v205, v204, s[58:59]
	s_nop 1
	v_permlane16_swap_b32_e32 v237, v238
	s_mov_b32 s58, -1
	s_mov_b32 s59, 0
	v_min_u32_e32 v202, v237, v238
	v_max_u32_e32 v203, v237, v238
	v_cndmask_b32_e64 v237, v203, v202, s[58:59]
	v_cndmask_b32_e64 v238, v202, v203, s[58:59]
	s_mov_b32 s58, 0xf0f0f0f
	s_mov_b32 s59, 0xf0f0f0f0
	v_mov_b32_dpp v202, v237 row_half_mirror row_mask:0xf bank_mask:0xf
	v_mov_b32_dpp v204, v238 row_half_mirror row_mask:0xf bank_mask:0xf
	s_nop 0
	v_max_u32_dpp v203, v202, v237 quad_perm:[3,2,1,0] row_mask:0xf bank_mask:0xf
	v_max_u32_dpp v205, v204, v238 quad_perm:[3,2,1,0] row_mask:0xf bank_mask:0xf
	v_min_u32_dpp v202, v202, v237 quad_perm:[3,2,1,0] row_mask:0xf bank_mask:0xf
	v_min_u32_dpp v204, v204, v238 quad_perm:[3,2,1,0] row_mask:0xf bank_mask:0xf
	v_cndmask_b32_e64 v237, v203, v202, s[58:59]
	v_cndmask_b32_e64 v238, v205, v204, s[58:59]
	s_mov_b32 s58, 0xff00ff
	s_mov_b32 s59, 0xff00ff00
	v_min_u32_dpp v202, v237, v237 row_ror:8 row_mask:0xf bank_mask:0xf
	v_max_u32_dpp v203, v237, v237 row_ror:8 row_mask:0xf bank_mask:0xf
	v_min_u32_dpp v204, v238, v238 row_ror:8 row_mask:0xf bank_mask:0xf
	v_max_u32_dpp v205, v238, v238 row_ror:8 row_mask:0xf bank_mask:0xf
	v_cndmask_b32_e64 v237, v203, v202, s[58:59]
	v_cndmask_b32_e64 v238, v205, v204, s[58:59]
	s_mov_b32 s58, 0x33333333
	s_mov_b32 s59, 0xcccccccc
	v_min_u32_dpp v202, v237, v237 quad_perm:[2,3,0,1] row_mask:0xf bank_mask:0xf
	v_max_u32_dpp v203, v237, v237 quad_perm:[2,3,0,1] row_mask:0xf bank_mask:0xf
	v_min_u32_dpp v204, v238, v238 quad_perm:[2,3,0,1] row_mask:0xf bank_mask:0xf
	v_max_u32_dpp v205, v238, v238 quad_perm:[2,3,0,1] row_mask:0xf bank_mask:0xf
	v_cndmask_b32_e64 v237, v203, v202, s[58:59]
	v_cndmask_b32_e64 v238, v205, v204, s[58:59]
	s_mov_b32 s58, 0x55555555
	s_mov_b32 s59, 0xaaaaaaaa
	v_min_u32_dpp v202, v237, v237 quad_perm:[1,0,3,2] row_mask:0xf bank_mask:0xf
	v_max_u32_dpp v203, v237, v237 quad_perm:[1,0,3,2] row_mask:0xf bank_mask:0xf
	v_min_u32_dpp v204, v238, v238 quad_perm:[1,0,3,2] row_mask:0xf bank_mask:0xf
	v_max_u32_dpp v205, v238, v238 quad_perm:[1,0,3,2] row_mask:0xf bank_mask:0xf
	v_cndmask_b32_e64 v237, v203, v202, s[58:59]
	v_cndmask_b32_e64 v238, v205, v204, s[58:59]
	s_nop 1
	v_permlane32_swap_b32_e32 v237, v238
	s_mov_b32 s58, 0xffff
	s_mov_b32 s59, 0xffff
	v_min_u32_e32 v202, v237, v238
	v_max_u32_e32 v203, v237, v238
	v_cndmask_b32_e64 v237, v203, v202, s[58:59]
	v_cndmask_b32_e64 v238, v202, v203, s[58:59]
	s_nop 1
	v_permlane32_swap_b32_e32 v237, v238
	s_mov_b32 s58, 0xffff
	s_mov_b32 s59, 0xffff
	v_min_u32_e32 v202, v237, v238
	v_max_u32_e32 v203, v237, v238
	v_cndmask_b32_e64 v237, v203, v202, s[58:59]
	v_cndmask_b32_e64 v238, v202, v203, s[58:59]
	s_mov_b32 s58, 0xf0f00f0f
	s_mov_b32 s59, 0xf0f00f0f
	v_mov_b32_dpp v202, v237 row_half_mirror row_mask:0xf bank_mask:0xf
	v_mov_b32_dpp v204, v238 row_half_mirror row_mask:0xf bank_mask:0xf
	s_nop 0
	v_max_u32_dpp v203, v202, v237 quad_perm:[3,2,1,0] row_mask:0xf bank_mask:0xf
	v_max_u32_dpp v205, v204, v238 quad_perm:[3,2,1,0] row_mask:0xf bank_mask:0xf
	v_min_u32_dpp v202, v202, v237 quad_perm:[3,2,1,0] row_mask:0xf bank_mask:0xf
	v_min_u32_dpp v204, v204, v238 quad_perm:[3,2,1,0] row_mask:0xf bank_mask:0xf
	v_cndmask_b32_e64 v237, v203, v202, s[58:59]
	v_cndmask_b32_e64 v238, v205, v204, s[58:59]
	s_mov_b32 s58, 0xff0000ff
	s_mov_b32 s59, 0xff0000ff
	v_min_u32_dpp v202, v237, v237 row_ror:8 row_mask:0xf bank_mask:0xf
	v_max_u32_dpp v203, v237, v237 row_ror:8 row_mask:0xf bank_mask:0xf
	v_min_u32_dpp v204, v238, v238 row_ror:8 row_mask:0xf bank_mask:0xf
	v_max_u32_dpp v205, v238, v238 row_ror:8 row_mask:0xf bank_mask:0xf
	v_cndmask_b32_e64 v237, v203, v202, s[58:59]
	v_cndmask_b32_e64 v238, v205, v204, s[58:59]
	s_mov_b32 s58, 0xcccc3333
	s_mov_b32 s59, 0xcccc3333
	v_min_u32_dpp v202, v237, v237 quad_perm:[2,3,0,1] row_mask:0xf bank_mask:0xf
; __device__ __forceinline__ void expert_tokens(const unsigned char* __restrict__ UV, const float* __restrict__ US, const float* __restrict__ VS, ...
;     ...
;             if (bi == 0) { nsu0 = US[ni0]; nsu1 = US[ni1]; nsv0 = VS[ni0]; nsv1 = VS[ni1]; }
	v_max_u32_dpp v203, v237, v237 quad_perm:[2,3,0,1] row_mask:0xf bank_mask:0xf
	v_min_u32_dpp v204, v238, v238 quad_perm:[2,3,0,1] row_mask:0xf bank_mask:0xf
	v_max_u32_dpp v205, v238, v238 quad_perm:[2,3,0,1] row_mask:0xf bank_mask:0xf
	v_cndmask_b32_e64 v237, v203, v202, s[58:59]
	v_cndmask_b32_e64 v238, v205, v204, s[58:59]
	s_mov_b32 s58, 0xaaaa5555
	s_mov_b32 s59, 0xaaaa5555
	v_min_u32_dpp v202, v237, v237 quad_perm:[1,0,3,2] row_mask:0xf bank_mask:0xf
	v_max_u32_dpp v203, v237, v237 quad_perm:[1,0,3,2] row_mask:0xf bank_mask:0xf
	v_min_u32_dpp v204, v238, v238 quad_perm:[1,0,3,2] row_mask:0xf bank_mask:0xf
	v_max_u32_dpp v205, v238, v238 quad_perm:[1,0,3,2] row_mask:0xf bank_mask:0xf
	v_cndmask_b32_e64 v237, v203, v202, s[58:59]
	v_cndmask_b32_e64 v238, v205, v204, s[58:59]
	s_nop 1
	v_permlane16_swap_b32_e32 v237, v238
	v_min_u32_e32 v202, v237, v238
	v_max_u32_e32 v238, v237, v238
	v_mov_b32_e32 v237, v202
	s_nop 1
	v_permlane32_swap_b32_e32 v237, v238
	v_min_u32_e32 v202, v237, v238
	v_max_u32_e32 v238, v237, v238
	v_mov_b32_e32 v237, v202
	s_nop 1
	v_permlane16_swap_b32_e32 v237, v238
	v_min_u32_e32 v202, v237, v238
	v_max_u32_e32 v238, v237, v238
	v_mov_b32_e32 v237, v202
	s_mov_b32 s58, 0xf0f0f0f
	s_mov_b32 s59, 0xf0f0f0f
	v_mov_b32_dpp v202, v237 row_half_mirror row_mask:0xf bank_mask:0xf
	v_mov_b32_dpp v204, v238 row_half_mirror row_mask:0xf bank_mask:0xf
	s_nop 0
	v_max_u32_dpp v203, v202, v237 quad_perm:[3,2,1,0] row_mask:0xf bank_mask:0xf
	v_max_u32_dpp v205, v204, v238 quad_perm:[3,2,1,0] row_mask:0xf bank_mask:0xf
	v_min_u32_dpp v202, v202, v237 quad_perm:[3,2,1,0] row_mask:0xf bank_mask:0xf
	v_min_u32_dpp v204, v204, v238 quad_perm:[3,2,1,0] row_mask:0xf bank_mask:0xf
	v_cndmask_b32_e64 v237, v203, v202, s[58:59]
	v_cndmask_b32_e64 v238, v205, v204, s[58:59]
	s_mov_b32 s58, 0xff00ff
	s_mov_b32 s59, 0xff00ff
	v_min_u32_dpp v202, v237, v237 row_ror:8 row_mask:0xf bank_mask:0xf
	v_max_u32_dpp v203, v237, v237 row_ror:8 row_mask:0xf bank_mask:0xf
	v_min_u32_dpp v204, v238, v238 row_ror:8 row_mask:0xf bank_mask:0xf
	v_max_u32_dpp v205, v238, v238 row_ror:8 row_mask:0xf bank_mask:0xf
	v_cndmask_b32_e64 v237, v203, v202, s[58:59]
	v_cndmask_b32_e64 v238, v205, v204, s[58:59]
	s_mov_b32 s58, 0x33333333
	s_mov_b32 s59, 0x33333333
	v_min_u32_dpp v202, v237, v237 quad_perm:[2,3,0,1] row_mask:0xf bank_mask:0xf
	v_max_u32_dpp v203, v237, v237 quad_perm:[2,3,0,1] row_mask:0xf bank_mask:0xf
	v_min_u32_dpp v204, v238, v238 quad_perm:[2,3,0,1] row_mask:0xf bank_mask:0xf
	v_max_u32_dpp v205, v238, v238 quad_perm:[2,3,0,1] row_mask:0xf bank_mask:0xf
	v_cndmask_b32_e64 v237, v203, v202, s[58:59]
	v_cndmask_b32_e64 v238, v205, v204, s[58:59]
	s_mov_b32 s58, 0x55555555
	s_mov_b32 s59, 0x55555555
	v_min_u32_dpp v202, v237, v237 quad_perm:[1,0,3,2] row_mask:0xf bank_mask:0xf
	v_max_u32_dpp v203, v237, v237 quad_perm:[1,0,3,2] row_mask:0xf bank_mask:0xf
	v_min_u32_dpp v204, v238, v238 quad_perm:[1,0,3,2] row_mask:0xf bank_mask:0xf
	v_max_u32_dpp v205, v238, v238 quad_perm:[1,0,3,2] row_mask:0xf bank_mask:0xf
	v_cndmask_b32_e64 v237, v203, v202, s[58:59]
	v_cndmask_b32_e64 v238, v205, v204, s[58:59]
	s_nop 1
	v_permlane16_swap_b32_e32 v237, v238
	s_nop 1
	v_permlane32_swap_b32_e32 v237, v238
	v_xor_b32_e32 v237, s60, v237
	v_xor_b32_e32 v238, s60, v238
	v_alignbit_b32 v237, v237, v237, 16
	v_alignbit_b32 v238, v238, v238, 16
	v_and_b32_e32 v242, 0x3fff, v237
	v_and_b32_e32 v243, 0x3fff, v238
	v_lshlrev_b32_e32 v208, 2, v242
	v_lshlrev_b32_e32 v206, 2, v243
	global_load_dword v241, v208, s[12:13]
	global_load_dword v0, v206, s[12:13]
	global_load_dword v245, v208, s[14:15]
	global_load_dword v246, v206, s[14:15]
.LBB0_1021:
	v_perm_b32 v149, v186, v190, s29
	v_dot2c_f32_f16_e32 v224, s47, v149
	v_and_b32_e32 v149, 0xf000f0, v149
	v_dot2c_f32_f16_e32 v220, s47, v149
	v_perm_b32 v149, v186, v190, s30
	v_dot2c_f32_f16_e32 v225, s47, v149
	v_and_b32_e32 v149, 0xf000f0, v149
	v_dot2c_f32_f16_e32 v221, s47, v149
	v_perm_b32 v149, v186, v190, s31
	v_perm_b32 v117, v186, v190, s33
	v_dot2c_f32_f16_e32 v223, s47, v117
	v_and_b32_e32 v117, 0xf000f0, v117
	v_dot2c_f32_f16_e32 v222, s47, v149
	v_and_b32_e32 v149, 0xf000f0, v149
	v_dot2c_f32_f16_e32 v219, s47, v117
	v_dot2c_f32_f16_e32 v218, s47, v149
	v_perm_b32 v149, v187, v191, s29
	v_dot2c_f32_f16_e32 v216, s47, v149
	v_and_b32_e32 v149, 0xf000f0, v149
	v_dot2c_f32_f16_e32 v212, s47, v149
	v_perm_b32 v149, v187, v191, s30
	v_dot2c_f32_f16_e32 v217, s47, v149
	v_and_b32_e32 v149, 0xf000f0, v149
	v_dot2c_f32_f16_e32 v213, s47, v149
	v_perm_b32 v149, v187, v191, s31
	v_perm_b32 v117, v187, v191, s33
	v_dot2c_f32_f16_e32 v215, s47, v117
	v_and_b32_e32 v117, 0xf000f0, v117
	v_dot2c_f32_f16_e32 v214, s47, v149
	v_and_b32_e32 v149, 0xf000f0, v149
	v_dot2c_f32_f16_e32 v211, s47, v117
	v_dot2c_f32_f16_e32 v210, s47, v149
	v_perm_b32 v149, v178, v182, s29
	v_dot2c_f32_f16_e32 v224, s45, v149
	v_and_b32_e32 v149, 0xf000f0, v149
	v_dot2c_f32_f16_e32 v220, s45, v149
	v_perm_b32 v149, v178, v182, s30
	v_dot2c_f32_f16_e32 v225, s45, v149
	v_and_b32_e32 v149, 0xf000f0, v149
	v_dot2c_f32_f16_e32 v221, s45, v149
	v_perm_b32 v149, v178, v182, s31
	v_perm_b32 v117, v178, v182, s33
	v_dot2c_f32_f16_e32 v223, s45, v117
	v_and_b32_e32 v117, 0xf000f0, v117
	v_dot2c_f32_f16_e32 v222, s45, v149
	v_and_b32_e32 v149, 0xf000f0, v149
	v_dot2c_f32_f16_e32 v219, s45, v117
	v_dot2c_f32_f16_e32 v218, s45, v149
	v_perm_b32 v149, v179, v183, s29
	v_dot2c_f32_f16_e32 v216, s45, v149
	v_and_b32_e32 v149, 0xf000f0, v149
	v_dot2c_f32_f16_e32 v212, s45, v149
	v_perm_b32 v149, v179, v183, s30
	v_dot2c_f32_f16_e32 v217, s45, v149
	v_and_b32_e32 v149, 0xf000f0, v149
	v_dot2c_f32_f16_e32 v213, s45, v149
	v_perm_b32 v149, v179, v183, s31
	v_perm_b32 v117, v179, v183, s33
	v_dot2c_f32_f16_e32 v215, s45, v117
	v_and_b32_e32 v117, 0xf000f0, v117
	v_dot2c_f32_f16_e32 v214, s45, v149
	v_and_b32_e32 v149, 0xf000f0, v149
	v_dot2c_f32_f16_e32 v211, s45, v117
	v_dot2c_f32_f16_e32 v210, s45, v149
	v_perm_b32 v149, v170, v174, s29
	v_dot2c_f32_f16_e32 v224, s43, v149
	v_and_b32_e32 v149, 0xf000f0, v149
	v_dot2c_f32_f16_e32 v220, s43, v149
	v_perm_b32 v149, v170, v174, s30
	v_dot2c_f32_f16_e32 v225, s43, v149
	v_and_b32_e32 v149, 0xf000f0, v149
	v_dot2c_f32_f16_e32 v221, s43, v149
	v_perm_b32 v149, v170, v174, s31
	v_perm_b32 v117, v170, v174, s33
	v_dot2c_f32_f16_e32 v223, s43, v117
	v_and_b32_e32 v117, 0xf000f0, v117
	v_dot2c_f32_f16_e32 v222, s43, v149
	v_and_b32_e32 v149, 0xf000f0, v149
	v_dot2c_f32_f16_e32 v219, s43, v117
	v_dot2c_f32_f16_e32 v218, s43, v149
	v_perm_b32 v149, v171, v175, s29
	v_dot2c_f32_f16_e32 v216, s43, v149
	v_and_b32_e32 v149, 0xf000f0, v149
	v_dot2c_f32_f16_e32 v212, s43, v149
	v_perm_b32 v149, v171, v175, s30
	v_dot2c_f32_f16_e32 v217, s43, v149
	v_and_b32_e32 v149, 0xf000f0, v149
	v_dot2c_f32_f16_e32 v213, s43, v149
	v_perm_b32 v149, v171, v175, s31
	v_perm_b32 v117, v171, v175, s33
	v_dot2c_f32_f16_e32 v215, s43, v117
	v_and_b32_e32 v117, 0xf000f0, v117
	v_dot2c_f32_f16_e32 v214, s43, v149
	v_and_b32_e32 v149, 0xf000f0, v149
	v_dot2c_f32_f16_e32 v211, s43, v117
	v_dot2c_f32_f16_e32 v210, s43, v149
	v_perm_b32 v149, v162, v166, s29
	v_dot2c_f32_f16_e32 v224, s41, v149
	v_and_b32_e32 v149, 0xf000f0, v149
	v_dot2c_f32_f16_e32 v220, s41, v149
	v_perm_b32 v149, v162, v166, s30
	v_dot2c_f32_f16_e32 v225, s41, v149
	v_and_b32_e32 v149, 0xf000f0, v149
	v_dot2c_f32_f16_e32 v221, s41, v149
	v_perm_b32 v149, v162, v166, s31
	v_perm_b32 v117, v162, v166, s33
	v_dot2c_f32_f16_e32 v223, s41, v117
	v_and_b32_e32 v117, 0xf000f0, v117
	v_dot2c_f32_f16_e32 v222, s41, v149
	v_and_b32_e32 v149, 0xf000f0, v149
	v_dot2c_f32_f16_e32 v219, s41, v117
	v_dot2c_f32_f16_e32 v218, s41, v149
	v_perm_b32 v149, v163, v167, s29
	v_dot2c_f32_f16_e32 v216, s41, v149
	v_and_b32_e32 v149, 0xf000f0, v149
	v_dot2c_f32_f16_e32 v212, s41, v149
	v_perm_b32 v149, v163, v167, s30
	v_dot2c_f32_f16_e32 v217, s41, v149
	v_and_b32_e32 v149, 0xf000f0, v149
	v_dot2c_f32_f16_e32 v213, s41, v149
	v_perm_b32 v149, v163, v167, s31
	v_perm_b32 v117, v163, v167, s33
	v_dot2c_f32_f16_e32 v215, s41, v117
	v_and_b32_e32 v117, 0xf000f0, v117
	v_dot2c_f32_f16_e32 v214, s41, v149
	v_and_b32_e32 v149, 0xf000f0, v149
	v_dot2c_f32_f16_e32 v211, s41, v117
	v_dot2c_f32_f16_e32 v210, s41, v149
	v_perm_b32 v149, v154, v158, s29
	v_dot2c_f32_f16_e32 v224, s39, v149
	v_and_b32_e32 v149, 0xf000f0, v149
	v_dot2c_f32_f16_e32 v220, s39, v149
	v_perm_b32 v149, v154, v158, s30
	v_dot2c_f32_f16_e32 v225, s39, v149
	v_and_b32_e32 v149, 0xf000f0, v149
	v_dot2c_f32_f16_e32 v221, s39, v149
	v_perm_b32 v149, v154, v158, s31
	v_perm_b32 v117, v154, v158, s33
	v_dot2c_f32_f16_e32 v223, s39, v117
	v_and_b32_e32 v117, 0xf000f0, v117
	v_dot2c_f32_f16_e32 v222, s39, v149
	v_and_b32_e32 v149, 0xf000f0, v149
	v_dot2c_f32_f16_e32 v219, s39, v117
	v_dot2c_f32_f16_e32 v218, s39, v149
	v_perm_b32 v149, v155, v159, s29
	v_dot2c_f32_f16_e32 v216, s39, v149
	v_and_b32_e32 v149, 0xf000f0, v149
	v_dot2c_f32_f16_e32 v212, s39, v149
	v_perm_b32 v149, v155, v159, s30
	v_dot2c_f32_f16_e32 v217, s39, v149
	v_and_b32_e32 v149, 0xf000f0, v149
	v_dot2c_f32_f16_e32 v213, s39, v149
	v_perm_b32 v149, v155, v159, s31
	v_perm_b32 v117, v155, v159, s33
	v_dot2c_f32_f16_e32 v215, s39, v117
	v_and_b32_e32 v117, 0xf000f0, v117
	v_dot2c_f32_f16_e32 v214, s39, v149
	v_and_b32_e32 v149, 0xf000f0, v149
	v_dot2c_f32_f16_e32 v211, s39, v117
	v_perm_b32 v148, v146, v150, s29
	v_dot2c_f32_f16_e32 v224, s37, v148
	v_and_b32_e32 v148, 0xf000f0, v148
	v_dot2c_f32_f16_e32 v220, s37, v148
	v_perm_b32 v148, v146, v150, s30
	v_dot2c_f32_f16_e32 v225, s37, v148
	v_and_b32_e32 v148, 0xf000f0, v148
	v_dot2c_f32_f16_e32 v221, s37, v148
	v_perm_b32 v148, v146, v150, s31
	v_perm_b32 v117, v146, v150, s33
	v_dot2c_f32_f16_e32 v223, s37, v117
	v_and_b32_e32 v117, 0xf000f0, v117
	v_dot2c_f32_f16_e32 v222, s37, v148
	v_and_b32_e32 v148, 0xf000f0, v148
	v_dot2c_f32_f16_e32 v219, s37, v117
	v_perm_b32 v207, v147, v151, s29
	v_dot2c_f32_f16_e32 v216, s37, v207
	v_and_b32_e32 v207, 0xf000f0, v207
	v_dot2c_f32_f16_e32 v212, s37, v207
	v_perm_b32 v207, v147, v151, s30
	v_dot2c_f32_f16_e32 v217, s37, v207
	v_and_b32_e32 v207, 0xf000f0, v207
	v_dot2c_f32_f16_e32 v213, s37, v207
	v_perm_b32 v207, v147, v151, s31
	v_perm_b32 v117, v147, v151, s33
	v_dot2c_f32_f16_e32 v215, s37, v117
	v_and_b32_e32 v117, 0xf000f0, v117
	v_dot2c_f32_f16_e32 v214, s37, v207
	v_and_b32_e32 v207, 0xf000f0, v207
	v_dot2c_f32_f16_e32 v211, s37, v117
	v_perm_b32 v145, v114, v118, s29
	v_dot2c_f32_f16_e32 v224, s35, v145
	v_and_b32_e32 v145, 0xf000f0, v145
	v_dot2c_f32_f16_e32 v220, s35, v145
	v_perm_b32 v145, v114, v118, s30
	v_dot2c_f32_f16_e32 v225, s35, v145
	v_and_b32_e32 v145, 0xf000f0, v145
	v_dot2c_f32_f16_e32 v221, s35, v145
	v_perm_b32 v145, v114, v118, s31
	v_dot2c_f32_f16_e32 v222, s35, v145
	v_and_b32_e32 v145, 0xf000f0, v145
	v_perm_b32 v117, v114, v118, s33
	v_and_b32_e32 v209, 0xf000f0, v117
	v_dot2c_f32_f16_e32 v223, s35, v117
	v_dot2c_f32_f16_e32 v219, s35, v209
	v_perm_b32 v253, v115, v119, s29
	v_dot2c_f32_f16_e32 v216, s35, v253
	v_and_b32_e32 v253, 0xf000f0, v253
	v_dot2c_f32_f16_e32 v212, s35, v253
	v_perm_b32 v253, v115, v119, s30
	v_dot2c_f32_f16_e32 v217, s35, v253
	v_and_b32_e32 v253, 0xf000f0, v253
	v_dot2c_f32_f16_e32 v213, s35, v253
	v_perm_b32 v253, v115, v119, s31
	v_perm_b32 v209, v115, v119, s33
	v_dot2c_f32_f16_e32 v215, s35, v209
	v_and_b32_e32 v209, 0xf000f0, v209
	v_dot2c_f32_f16_e32 v214, s35, v253
	v_and_b32_e32 v253, 0xf000f0, v253
	v_dot2c_f32_f16_e32 v211, s35, v209
	v_perm_b32 v117, v68, v72, s29
	v_dot2c_f32_f16_e32 v224, s4, v117
	v_and_b32_e32 v117, 0xf000f0, v117
	v_dot2c_f32_f16_e32 v220, s4, v117
	v_perm_b32 v117, v68, v72, s30
	v_dot2c_f32_f16_e32 v225, s4, v117
	v_and_b32_e32 v117, 0xf000f0, v117
	v_dot2c_f32_f16_e32 v221, s4, v117
	v_perm_b32 v117, v68, v72, s31
	v_dot2c_f32_f16_e32 v222, s4, v117
	v_and_b32_e32 v117, 0xf000f0, v117
	v_perm_b32 v254, v68, v72, s33
	v_and_b32_e32 v254, 0xf000f0, v254
	v_perm_b32 v209, v68, v72, s33
	v_dot2c_f32_f16_e32 v219, s4, v254
	v_dot2c_f32_f16_e32 v223, s4, v209
	v_perm_b32 v209, v69, v73, s29
	v_dot2c_f32_f16_e32 v216, s4, v209
	v_and_b32_e32 v209, 0xf000f0, v209
	v_dot2c_f32_f16_e32 v212, s4, v209
	v_perm_b32 v209, v69, v73, s30
	v_dot2c_f32_f16_e32 v217, s4, v209
	v_and_b32_e32 v209, 0xf000f0, v209
	v_dot2c_f32_f16_e32 v213, s4, v209
	v_perm_b32 v209, v69, v73, s31
	v_perm_b32 v254, v69, v73, s33
	v_dot2c_f32_f16_e32 v215, s4, v254
	s_waitcnt vmcnt(31)
; __device__ __forceinline__ float gelu_as(float v) {
;     const float av = fabsf(v), t = __builtin_amdgcn_rcpf(av * 0.2316418882f + 1.0f);
;     float q = t * 0.5307027145f + (-0.7265760135f); q = q * t + 0.7107068705f; q = q * t + (-0.142248368f); q = q * t + 0.127414796f; q = q * t;
;     const float m = v * (q * __builtin_amdgcn_exp2f((v * v) * (-0.72134752044f)));
;     return v < 0.f ? m : v - m;
	v_dot8_i32_i4 v68, v248, v62, 0
	v_dot8_i32_i4 v68, v250, v63, v68
	v_dot2c_f32_f16_e32 v210, s39, v149
	v_dot2c_f32_f16_e32 v218, s37, v148
	v_dot2c_f32_f16_e32 v210, s37, v207
	v_lshlrev_b32_e32 v68, 4, v68
	v_dot8_i32_i4 v68, v247, v62, v68
	s_waitcnt vmcnt(30)
	v_dot8_i32_i4 v62, v248, v58, 0
	v_dot8_i32_i4 v62, v250, v59, v62
	v_dot8_i32_i4 v68, v249, v63, v68
	v_dot2c_f32_f16_e32 v218, s35, v145
	v_dot2c_f32_f16_e32 v210, s35, v253
	v_lshlrev_b32_e32 v62, 4, v62
	v_dot8_i32_i4 v62, v247, v58, v62
	s_waitcnt vmcnt(29)
	v_dot8_i32_i4 v58, v248, v54, 0
	v_dot8_i32_i4 v58, v250, v55, v58
	v_dot8_i32_i4 v62, v249, v59, v62
	v_dot2c_f32_f16_e32 v214, s4, v209
	v_and_b32_e32 v209, 0xf000f0, v209
	v_lshlrev_b32_e32 v58, 4, v58
	v_dot8_i32_i4 v58, v247, v54, v58
	s_waitcnt vmcnt(28)
	v_dot8_i32_i4 v54, v248, v50, 0
	v_dot8_i32_i4 v54, v250, v51, v54
	v_dot8_i32_i4 v58, v249, v55, v58
	v_dot2c_f32_f16_e32 v218, s4, v117
	v_dot2c_f32_f16_e32 v210, s4, v209
	v_lshlrev_b32_e32 v54, 4, v54
	v_dot8_i32_i4 v54, v247, v50, v54
	s_waitcnt vmcnt(27)
	v_dot8_i32_i4 v50, v248, v46, 0
	v_dot8_i32_i4 v50, v250, v47, v50
	v_dot8_i32_i4 v54, v249, v51, v54
	s_add_i32 s24, s25, 2
	s_cmp_lt_u32 s25, 5
	v_lshlrev_b32_e32 v50, 4, v50
	v_dot8_i32_i4 v50, v247, v46, v50
	s_waitcnt vmcnt(26)
	v_dot8_i32_i4 v46, v248, v42, 0
	v_dot8_i32_i4 v46, v250, v43, v46
	v_dot8_i32_i4 v50, v249, v47, v50
	v_cvt_f32_f16_e32 v116, v116
	s_nop 0
	v_lshlrev_b32_e32 v46, 4, v46
	v_dot8_i32_i4 v46, v247, v42, v46
	s_waitcnt vmcnt(25)
	v_dot8_i32_i4 v42, v248, v38, 0
	v_dot8_i32_i4 v42, v250, v39, v42
	v_dot8_i32_i4 v46, v249, v43, v46
	s_nop 1
	v_lshlrev_b32_e32 v42, 4, v42
	v_dot8_i32_i4 v42, v247, v38, v42
	s_waitcnt vmcnt(24)
	v_dot8_i32_i4 v38, v248, v30, 0
	v_dot8_i32_i4 v38, v250, v31, v38
	v_dot8_i32_i4 v42, v249, v39, v42
	s_nop 1
	v_lshlrev_b32_e32 v38, 4, v38
	v_dot8_i32_i4 v38, v247, v30, v38
	v_dot8_i32_i4 v38, v249, v31, v38
	s_waitcnt vmcnt(22)
	v_dot8_i32_i4 v31, v248, v22, 0
	v_dot8_i32_i4 v31, v250, v23, v31
	v_dot8_i32_i4 v30, v248, v34, 0
	v_dot8_i32_i4 v30, v250, v35, v30
	s_nop 0
	v_lshlrev_b32_e32 v31, 4, v31
	v_dot8_i32_i4 v31, v247, v22, v31
	v_dot8_i32_i4 v31, v249, v23, v31
	s_waitcnt vmcnt(20)
	v_dot8_i32_i4 v23, v248, v14, 0
	v_dot8_i32_i4 v23, v250, v15, v23
	v_dot8_i32_i4 v22, v248, v26, 0
	v_dot8_i32_i4 v22, v250, v27, v22
	s_nop 0
	v_lshlrev_b32_e32 v23, 4, v23
	v_dot8_i32_i4 v23, v247, v14, v23
	v_dot8_i32_i4 v23, v249, v15, v23
	s_waitcnt vmcnt(18)
	v_dot8_i32_i4 v15, v248, v6, 0
	v_dot8_i32_i4 v15, v250, v7, v15
	v_dot8_i32_i4 v14, v248, v18, 0
	v_dot8_i32_i4 v14, v250, v19, v14
	s_nop 0
	v_lshlrev_b32_e32 v15, 4, v15
	v_dot8_i32_i4 v15, v247, v6, v15
	v_dot8_i32_i4 v15, v249, v7, v15
	s_waitcnt vmcnt(17)
	v_dot8_i32_i4 v6, v248, v10, 0
	s_waitcnt vmcnt(16)
	v_dot8_i32_i4 v7, v248, v2, 0
	v_dot8_i32_i4 v6, v250, v11, v6
	v_dot8_i32_i4 v7, v250, v3, v7
	v_lshlrev_b32_e32 v30, 4, v30
	v_lshlrev_b32_e32 v22, 4, v22
	v_lshlrev_b32_e32 v14, 4, v14
	v_lshlrev_b32_e32 v6, 4, v6
	v_lshlrev_b32_e32 v7, 4, v7
	v_dot8_i32_i4 v30, v247, v34, v30
	v_dot8_i32_i4 v22, v247, v26, v22
	v_dot8_i32_i4 v14, v247, v18, v14
	v_dot8_i32_i4 v6, v247, v10, v6
	v_dot8_i32_i4 v7, v247, v2, v7
	v_dot8_i32_i4 v30, v249, v35, v30
	v_dot8_i32_i4 v22, v249, v27, v22
	v_dot8_i32_i4 v14, v249, v19, v14
	v_dot8_i32_i4 v6, v249, v11, v6
	v_dot8_i32_i4 v7, v249, v3, v7
	v_permlane32_swap_b32_e32 v68, v30
	v_permlane32_swap_b32_e32 v62, v31
	v_permlane32_swap_b32_e32 v58, v22
	v_permlane32_swap_b32_e32 v54, v23
	v_permlane32_swap_b32_e32 v50, v14
	v_permlane32_swap_b32_e32 v46, v15
	v_permlane32_swap_b32_e32 v42, v6
	v_permlane32_swap_b32_e32 v38, v7
	v_add_u32_e32 v2, v68, v30
	v_add_u32_e32 v3, v62, v31
	v_add_u32_e32 v10, v58, v22
	v_add_u32_e32 v11, v54, v23
	v_add_u32_e32 v14, v50, v14
	v_add_u32_e32 v15, v46, v15
	v_add_u32_e32 v6, v42, v6
	v_add_u32_e32 v7, v38, v7
	v_permlane16_swap_b32_e32 v2, v14
	v_permlane16_swap_b32_e32 v3, v15
	v_permlane16_swap_b32_e32 v10, v6
	v_permlane16_swap_b32_e32 v11, v7
	v_add_u32_e32 v2, v2, v14
	v_add_u32_e32 v3, v3, v15
	v_add_u32_e32 v6, v10, v6
	v_add_u32_e32 v7, v11, v7
	v_cndmask_b32_e64 v10, v6, v2, s[0:1]
	v_cndmask_b32_e64 v2, v2, v6, s[0:1]
	v_cndmask_b32_e64 v6, v7, v3, s[0:1]
	v_cndmask_b32_e64 v3, v3, v7, s[0:1]
	v_add_u32_dpp v2, v2, v10 quad_perm:[2,3,0,1] row_mask:0xf bank_mask:0xf bound_ctrl:1
	ds_bpermute_b32 v7, v66, v71 offset:64
	v_add_u32_dpp v3, v3, v6 quad_perm:[2,3,0,1] row_mask:0xf bank_mask:0xf bound_ctrl:1
	v_cndmask_b32_e64 v6, v3, v2, s[2:3]
	v_cndmask_b32_e64 v2, v2, v3, s[2:3]
	ds_bpermute_b32 v3, v66, v70 offset:64
	v_add_f32_e32 v68, v252, v116
	v_add_u32_dpp v2, v2, v6 quad_perm:[1,0,3,2] row_mask:0xf bank_mask:0xf bound_ctrl:1
	v_and_b32_e32 v6, 0xf000f0, v254
	v_dot2c_f32_f16_e32 v211, s4, v6
	v_add_u32_dpp v2, v2, v2 row_ror:8 row_mask:0xf bank_mask:0xf bound_ctrl:1
	ds_bpermute_b32 v6, v66, v67 offset:64
	s_nop 0
	v_add_u32_dpp v2, v2, v2 row_ror:4 row_mask:0xf bank_mask:0xf bound_ctrl:1
	v_cvt_f32_i32_e32 v2, v2
	v_add_f32_e32 v2, v251, v2
	v_mul_f32_e32 v2, v244, v2
	s_waitcnt lgkmcnt(1)
	v_mul_f32_e32 v2, v2, v3
	v_fma_f32 v3, |v2|, s28, 1.0
	v_rcp_f32_e32 v3, v3
	v_mul_f32_e32 v11, v2, v2
	v_mul_f32_e32 v11, 0xbf38aa3b, v11
	v_exp_f32_e32 v11, v11
	v_fmamk_f32 v10, v3, 0x3f07dc22, v227
	v_fmaak_f32 v10, v3, v10, 0x3f35f0e3
	v_fmaak_f32 v10, v3, v10, 0xbe11a98e
	v_fmaak_f32 v10, v3, v10, 0x3e027906
	v_mul_f32_e32 v3, v3, v10
	v_mul_f32_e32 v3, v11, v3
	v_mul_f32_e32 v10, v2, v3
	v_fma_f32 v3, -v2, v3, v2
	v_cmp_gt_f32_e64 s[4:5], 0, v2
	s_nop 1
	v_cndmask_b32_e64 v2, v3, v10, s[4:5]
	s_waitcnt lgkmcnt(0)
	v_mul_f32_e32 v2, v2, v6
	v_mul_f32_e32 v2, v2, v7
	v_fma_mixlo_f16 v2, v2, s16, 0
	v_and_b32_e32 v3, 0xffff, v2
	s_cselect_b64 s[4:5], -1, 0
	s_nop 0
	v_mov_b32_dpp v253, v3 quad_perm:[1,0,3,2] row_mask:0xf bank_mask:0xf
	v_lshl_or_b32 v254, v253, 16, v3
	v_cvt_f32_f16_e32 v66, v2
	v_cndmask_b32_e64 v2, v242, v232, s[4:5]
	v_readlane_b32 s5, v254, 0
	v_perm_b32 v14, v60, v64, s29
	s_nop 0
	v_dot2c_f32_f16_e32 v224, s5, v14
	v_and_b32_e32 v14, 0xf000f0, v14
	v_dot2c_f32_f16_e32 v220, s5, v14
	v_perm_b32 v14, v60, v64, s30
	v_dot2c_f32_f16_e32 v225, s5, v14
	v_and_b32_e32 v14, 0xf000f0, v14
	v_dot2c_f32_f16_e32 v221, s5, v14
	v_perm_b32 v14, v60, v64, s31
	v_perm_b32 v6, v60, v64, s33
	v_dot2c_f32_f16_e32 v223, s5, v6
	v_and_b32_e32 v6, 0xf000f0, v6
	v_dot2c_f32_f16_e32 v222, s5, v14
	v_and_b32_e32 v14, 0xf000f0, v14
	v_dot2c_f32_f16_e32 v219, s5, v6
	v_dot2c_f32_f16_e32 v218, s5, v14
	v_perm_b32 v14, v61, v65, s29
	v_dot2c_f32_f16_e32 v216, s5, v14
	v_and_b32_e32 v14, 0xf000f0, v14
	v_dot2c_f32_f16_e32 v212, s5, v14
	v_perm_b32 v14, v61, v65, s30
	v_dot2c_f32_f16_e32 v217, s5, v14
	v_and_b32_e32 v14, 0xf000f0, v14
	v_dot2c_f32_f16_e32 v213, s5, v14
	v_perm_b32 v14, v61, v65, s31
	v_perm_b32 v6, v61, v65, s33
	v_dot2c_f32_f16_e32 v214, s5, v14
	v_and_b32_e32 v14, 0xf000f0, v14
	v_dot2c_f32_f16_e32 v215, s5, v6
	v_and_b32_e32 v6, 0xf000f0, v6
	v_cndmask_b32_e32 v2, v2, v231, vcc
	v_dot2c_f32_f16_e32 v210, s5, v14
	v_dot2c_f32_f16_e32 v211, s5, v6
	v_lshlrev_b32_e32 v2, 10, v2
	s_add_i32 s61, s21, 16
	v_readlane_b32 s61, v2, s61
	s_add_i32 s62, s21, 17
	v_readlane_b32 s62, v2, s62
	s_add_i32 s63, s21, 18
	v_readlane_b32 s63, v2, s63
	s_add_i32 s64, s21, 19
	v_readlane_b32 s64, v2, s64
	s_add_i32 s65, s21, 20
	v_readlane_b32 s65, v2, s65
	s_add_i32 s66, s21, 21
	v_readlane_b32 s66, v2, s66
	s_add_i32 s67, s21, 22
	v_readlane_b32 s67, v2, s67
	s_add_i32 s68, s21, 23
	v_readlane_b32 s68, v2, s68
	s_add_i32 s69, s21, 24
	v_readlane_b32 s69, v2, s69
	s_add_i32 s70, s21, 25
	v_readlane_b32 s70, v2, s70
	s_add_i32 s71, s21, 26
	v_readlane_b32 s71, v2, s71
	s_add_i32 s72, s21, 27
	v_readlane_b32 s72, v2, s72
	s_add_i32 s73, s21, 28
	v_readlane_b32 s73, v2, s73
	s_add_i32 s74, s21, 29
	v_readlane_b32 s74, v2, s74
	s_add_i32 s75, s21, 30
	v_readlane_b32 s75, v2, s75
	s_add_i32 s76, s21, 31
	v_readlane_b32 s76, v2, s76
	buffer_load_dwordx4 v[62:65], v194, s[80:83], s61 offen
	buffer_load_dwordx4 v[58:61], v194, s[80:83], s62 offen
	v_readlane_b32 s4, v254, 2
	v_perm_b32 v14, v52, v56, s29
	s_nop 0
	v_dot2c_f32_f16_e32 v224, s4, v14
	v_and_b32_e32 v14, 0xf000f0, v14
	v_dot2c_f32_f16_e32 v220, s4, v14
	v_perm_b32 v14, v52, v56, s30
	v_dot2c_f32_f16_e32 v225, s4, v14
	v_and_b32_e32 v14, 0xf000f0, v14
	v_dot2c_f32_f16_e32 v221, s4, v14
	v_perm_b32 v14, v52, v56, s31
	v_perm_b32 v6, v52, v56, s33
	v_dot2c_f32_f16_e32 v223, s4, v6
	v_and_b32_e32 v6, 0xf000f0, v6
	v_dot2c_f32_f16_e32 v222, s4, v14
	v_and_b32_e32 v14, 0xf000f0, v14
	v_dot2c_f32_f16_e32 v219, s4, v6
	v_dot2c_f32_f16_e32 v218, s4, v14
	v_perm_b32 v14, v53, v57, s29
	v_dot2c_f32_f16_e32 v216, s4, v14
	v_and_b32_e32 v14, 0xf000f0, v14
	v_dot2c_f32_f16_e32 v212, s4, v14
	v_perm_b32 v14, v53, v57, s30
	v_dot2c_f32_f16_e32 v217, s4, v14
	v_and_b32_e32 v14, 0xf000f0, v14
	v_dot2c_f32_f16_e32 v213, s4, v14
	v_perm_b32 v14, v53, v57, s31
	v_perm_b32 v6, v53, v57, s33
	v_dot2c_f32_f16_e32 v214, s4, v14
	v_and_b32_e32 v14, 0xf000f0, v14
	v_dot2c_f32_f16_e32 v215, s4, v6
	v_and_b32_e32 v6, 0xf000f0, v6
	v_dot2c_f32_f16_e32 v210, s4, v14
	v_dot2c_f32_f16_e32 v211, s4, v6
	buffer_load_dwordx4 v[54:57], v194, s[80:83], s63 offen
	buffer_load_dwordx4 v[50:53], v194, s[80:83], s64 offen
	v_readlane_b32 s4, v254, 16
	v_perm_b32 v14, v44, v48, s29
	s_nop 0
	v_dot2c_f32_f16_e32 v224, s4, v14
	v_and_b32_e32 v14, 0xf000f0, v14
	v_dot2c_f32_f16_e32 v220, s4, v14
	v_perm_b32 v14, v44, v48, s30
	v_dot2c_f32_f16_e32 v225, s4, v14
	v_and_b32_e32 v14, 0xf000f0, v14
	v_dot2c_f32_f16_e32 v221, s4, v14
	v_perm_b32 v14, v44, v48, s31
	v_perm_b32 v6, v44, v48, s33
	v_dot2c_f32_f16_e32 v223, s4, v6
	v_and_b32_e32 v6, 0xf000f0, v6
	v_dot2c_f32_f16_e32 v222, s4, v14
	v_and_b32_e32 v14, 0xf000f0, v14
	v_dot2c_f32_f16_e32 v219, s4, v6
	v_dot2c_f32_f16_e32 v218, s4, v14
	v_perm_b32 v14, v45, v49, s29
	v_dot2c_f32_f16_e32 v216, s4, v14
	v_and_b32_e32 v14, 0xf000f0, v14
	v_dot2c_f32_f16_e32 v212, s4, v14
	v_perm_b32 v14, v45, v49, s30
	v_dot2c_f32_f16_e32 v217, s4, v14
	v_and_b32_e32 v14, 0xf000f0, v14
	v_dot2c_f32_f16_e32 v213, s4, v14
	v_perm_b32 v14, v45, v49, s31
	v_perm_b32 v6, v45, v49, s33
	v_dot2c_f32_f16_e32 v214, s4, v14
	v_and_b32_e32 v14, 0xf000f0, v14
	v_dot2c_f32_f16_e32 v215, s4, v6
	v_and_b32_e32 v6, 0xf000f0, v6
	v_dot2c_f32_f16_e32 v210, s4, v14
	v_dot2c_f32_f16_e32 v211, s4, v6
	buffer_load_dwordx4 v[46:49], v194, s[80:83], s65 offen
	buffer_load_dwordx4 v[42:45], v194, s[80:83], s66 offen
	v_readlane_b32 s4, v254, 18
	v_perm_b32 v14, v32, v40, s29
	s_nop 0
	v_dot2c_f32_f16_e32 v224, s4, v14
	v_and_b32_e32 v14, 0xf000f0, v14
	v_dot2c_f32_f16_e32 v220, s4, v14
	v_perm_b32 v14, v32, v40, s30
	v_dot2c_f32_f16_e32 v225, s4, v14
	v_and_b32_e32 v14, 0xf000f0, v14
	v_dot2c_f32_f16_e32 v221, s4, v14
	v_perm_b32 v14, v32, v40, s31
	v_perm_b32 v6, v32, v40, s33
	v_dot2c_f32_f16_e32 v223, s4, v6
	v_and_b32_e32 v6, 0xf000f0, v6
	v_dot2c_f32_f16_e32 v222, s4, v14
	v_and_b32_e32 v14, 0xf000f0, v14
	v_dot2c_f32_f16_e32 v219, s4, v6
	v_dot2c_f32_f16_e32 v218, s4, v14
	v_perm_b32 v14, v33, v41, s29
	v_dot2c_f32_f16_e32 v216, s4, v14
	v_and_b32_e32 v14, 0xf000f0, v14
	v_dot2c_f32_f16_e32 v212, s4, v14
	v_perm_b32 v14, v33, v41, s30
; __device__ __forceinline__ void expert_tokens(const unsigned char* __restrict__ UV, const float* __restrict__ US, const float* __restrict__ VS, ...
;     ...
;         for (int bi = 0; bi < 128 / EB; bi += 2) {
;             EXP_STEP(A, bi);
;             if (bi == 0) { nsu0 = US[ni0]; nsu1 = US[ni1]; nsv0 = VS[ni0]; nsv1 = VS[ni1]; }
;             EXP_STEP(B, bi + 1);
;         }
	v_dot2c_f32_f16_e32 v217, s4, v14
	v_and_b32_e32 v14, 0xf000f0, v14
	v_dot2c_f32_f16_e32 v213, s4, v14
	v_perm_b32 v14, v33, v41, s31
	v_perm_b32 v6, v33, v41, s33
	v_dot2c_f32_f16_e32 v214, s4, v14
	v_and_b32_e32 v14, 0xf000f0, v14
	v_dot2c_f32_f16_e32 v215, s4, v6
	v_and_b32_e32 v6, 0xf000f0, v6
	v_dot2c_f32_f16_e32 v210, s4, v14
	v_dot2c_f32_f16_e32 v211, s4, v6
	buffer_load_dwordx4 v[38:41], v194, s[80:83], s67 offen
	buffer_load_dwordx4 v[30:33], v194, s[80:83], s68 offen
	v_readlane_b32 s4, v254, 32
	v_perm_b32 v14, v24, v36, s29
	s_nop 0
	v_dot2c_f32_f16_e32 v224, s4, v14
	v_and_b32_e32 v14, 0xf000f0, v14
	v_dot2c_f32_f16_e32 v220, s4, v14
	v_perm_b32 v14, v24, v36, s30
	v_dot2c_f32_f16_e32 v225, s4, v14
	v_and_b32_e32 v14, 0xf000f0, v14
	v_dot2c_f32_f16_e32 v221, s4, v14
	v_perm_b32 v14, v24, v36, s31
	v_perm_b32 v6, v24, v36, s33
	v_dot2c_f32_f16_e32 v223, s4, v6
	v_and_b32_e32 v6, 0xf000f0, v6
	v_dot2c_f32_f16_e32 v222, s4, v14
	v_and_b32_e32 v14, 0xf000f0, v14
	v_dot2c_f32_f16_e32 v219, s4, v6
	v_dot2c_f32_f16_e32 v218, s4, v14
	v_perm_b32 v14, v25, v37, s29
	v_dot2c_f32_f16_e32 v216, s4, v14
	v_and_b32_e32 v14, 0xf000f0, v14
	v_dot2c_f32_f16_e32 v212, s4, v14
	v_perm_b32 v14, v25, v37, s30
	v_dot2c_f32_f16_e32 v217, s4, v14
	v_and_b32_e32 v14, 0xf000f0, v14
	v_dot2c_f32_f16_e32 v213, s4, v14
	v_perm_b32 v14, v25, v37, s31
	v_perm_b32 v6, v25, v37, s33
	v_dot2c_f32_f16_e32 v214, s4, v14
	v_and_b32_e32 v14, 0xf000f0, v14
	v_dot2c_f32_f16_e32 v215, s4, v6
	v_and_b32_e32 v6, 0xf000f0, v6
	v_dot2c_f32_f16_e32 v210, s4, v14
	v_dot2c_f32_f16_e32 v211, s4, v6
	buffer_load_dwordx4 v[34:37], v194, s[80:83], s69 offen
	buffer_load_dwordx4 v[22:25], v194, s[80:83], s70 offen
	v_readlane_b32 s4, v254, 34
	v_perm_b32 v14, v16, v28, s29
	s_nop 0
	v_dot2c_f32_f16_e32 v224, s4, v14
	v_and_b32_e32 v14, 0xf000f0, v14
	v_dot2c_f32_f16_e32 v220, s4, v14
	v_perm_b32 v14, v16, v28, s30
	v_dot2c_f32_f16_e32 v225, s4, v14
	v_and_b32_e32 v14, 0xf000f0, v14
	v_dot2c_f32_f16_e32 v221, s4, v14
	v_perm_b32 v14, v16, v28, s31
	v_perm_b32 v6, v16, v28, s33
	v_dot2c_f32_f16_e32 v223, s4, v6
	v_and_b32_e32 v6, 0xf000f0, v6
	v_dot2c_f32_f16_e32 v222, s4, v14
	v_and_b32_e32 v14, 0xf000f0, v14
	v_dot2c_f32_f16_e32 v219, s4, v6
	v_dot2c_f32_f16_e32 v218, s4, v14
	v_perm_b32 v14, v17, v29, s29
	v_dot2c_f32_f16_e32 v216, s4, v14
	v_and_b32_e32 v14, 0xf000f0, v14
	v_dot2c_f32_f16_e32 v212, s4, v14
	v_perm_b32 v14, v17, v29, s30
	v_dot2c_f32_f16_e32 v217, s4, v14
	v_and_b32_e32 v14, 0xf000f0, v14
	v_dot2c_f32_f16_e32 v213, s4, v14
	v_perm_b32 v14, v17, v29, s31
	v_perm_b32 v6, v17, v29, s33
	v_dot2c_f32_f16_e32 v214, s4, v14
	v_and_b32_e32 v14, 0xf000f0, v14
	v_dot2c_f32_f16_e32 v215, s4, v6
	v_and_b32_e32 v6, 0xf000f0, v6
	v_dot2c_f32_f16_e32 v210, s4, v14
	v_dot2c_f32_f16_e32 v211, s4, v6
	buffer_load_dwordx4 v[26:29], v194, s[80:83], s71 offen
	buffer_load_dwordx4 v[14:17], v194, s[80:83], s72 offen
	v_readlane_b32 s4, v254, 48
	v_perm_b32 v11, v8, v20, s29
	s_nop 0
	v_dot2c_f32_f16_e32 v224, s4, v11
	v_and_b32_e32 v11, 0xf000f0, v11
	v_dot2c_f32_f16_e32 v220, s4, v11
	v_perm_b32 v11, v8, v20, s30
	v_dot2c_f32_f16_e32 v225, s4, v11
	v_and_b32_e32 v11, 0xf000f0, v11
	v_dot2c_f32_f16_e32 v221, s4, v11
	v_perm_b32 v11, v8, v20, s31
	v_perm_b32 v6, v8, v20, s33
	v_dot2c_f32_f16_e32 v223, s4, v6
	v_and_b32_e32 v6, 0xf000f0, v6
	v_dot2c_f32_f16_e32 v222, s4, v11
	v_and_b32_e32 v11, 0xf000f0, v11
	v_dot2c_f32_f16_e32 v219, s4, v6
	v_perm_b32 v10, v9, v21, s29
	v_dot2c_f32_f16_e32 v216, s4, v10
	v_and_b32_e32 v10, 0xf000f0, v10
	v_dot2c_f32_f16_e32 v212, s4, v10
	v_perm_b32 v10, v9, v21, s30
	v_dot2c_f32_f16_e32 v217, s4, v10
	v_and_b32_e32 v10, 0xf000f0, v10
	v_dot2c_f32_f16_e32 v213, s4, v10
	v_perm_b32 v10, v9, v21, s31
	v_perm_b32 v6, v9, v21, s33
	v_dot2c_f32_f16_e32 v214, s4, v10
	v_and_b32_e32 v10, 0xf000f0, v10
	v_dot2c_f32_f16_e32 v215, s4, v6
	v_and_b32_e32 v6, 0xf000f0, v6
	v_dot2c_f32_f16_e32 v218, s4, v11
	v_dot2c_f32_f16_e32 v210, s4, v10
	v_dot2c_f32_f16_e32 v211, s4, v6
	buffer_load_dwordx4 v[18:21], v194, s[80:83], s73 offen
	buffer_load_dwordx4 v[6:9], v194, s[80:83], s74 offen
	v_readlane_b32 s4, v254, 50
	v_perm_b32 v254, v4, v12, s29
	s_nop 0
	v_dot2c_f32_f16_e32 v224, s4, v254
	v_and_b32_e32 v254, 0xf000f0, v254
	v_dot2c_f32_f16_e32 v220, s4, v254
	v_perm_b32 v254, v4, v12, s30
	v_dot2c_f32_f16_e32 v225, s4, v254
	v_and_b32_e32 v254, 0xf000f0, v254
	v_dot2c_f32_f16_e32 v221, s4, v254
	v_perm_b32 v254, v4, v12, s31
	v_perm_b32 v3, v4, v12, s33
	v_dot2c_f32_f16_e32 v223, s4, v3
	v_and_b32_e32 v3, 0xf000f0, v3
	v_dot2c_f32_f16_e32 v222, s4, v254
	v_and_b32_e32 v254, 0xf000f0, v254
	v_dot2c_f32_f16_e32 v219, s4, v3
	v_perm_b32 v11, v5, v13, s29
	v_dot2c_f32_f16_e32 v216, s4, v11
	v_and_b32_e32 v11, 0xf000f0, v11
	v_dot2c_f32_f16_e32 v212, s4, v11
	v_perm_b32 v11, v5, v13, s30
	v_dot2c_f32_f16_e32 v217, s4, v11
	v_and_b32_e32 v11, 0xf000f0, v11
	v_dot2c_f32_f16_e32 v213, s4, v11
	v_perm_b32 v11, v5, v13, s31
	v_perm_b32 v3, v5, v13, s33
	v_dot2c_f32_f16_e32 v214, s4, v11
	v_and_b32_e32 v11, 0xf000f0, v11
	v_dot2c_f32_f16_e32 v215, s4, v3
	v_and_b32_e32 v3, 0xf000f0, v3
	v_dot2c_f32_f16_e32 v218, s4, v254
	v_dot2c_f32_f16_e32 v210, s4, v11
	v_dot2c_f32_f16_e32 v211, s4, v3
	buffer_load_dwordx4 v[10:13], v194, s[80:83], s75 offen
	buffer_load_dwordx4 v[2:5], v194, s[80:83], s76 offen
	v_add_f32_e32 v252, v68, v66
	s_add_i32 s21, s21, 32
	s_and_b64 vcc, exec, s[22:23]
	s_cbranch_vccnz .LBB0_1013
	s_waitcnt vmcnt(23)
	v_mov_b64_e32 v[158:159], v[112:113]
	v_mov_b64_e32 v[190:191], v[80:81]
	v_mov_b64_e32 v[186:187], v[76:77]
	v_mov_b64_e32 v[182:183], v[88:89]
	v_mov_b64_e32 v[178:179], v[84:85]
	v_mov_b64_e32 v[174:175], v[96:97]
	v_mov_b64_e32 v[170:171], v[92:93]
	v_mov_b64_e32 v[166:167], v[104:105]
	v_mov_b64_e32 v[162:163], v[100:101]
	v_mov_b64_e32 v[156:157], v[110:111]
	s_waitcnt vmcnt(22)
	v_mov_b64_e32 v[154:155], v[108:109]
	s_waitcnt vmcnt(21)
	v_mov_b64_e32 v[150:151], v[126:127]
	s_waitcnt vmcnt(20)
	v_mov_b64_e32 v[146:147], v[122:123]
	s_waitcnt vmcnt(19)
	v_mov_b64_e32 v[116:117], v[132:133]
	s_waitcnt vmcnt(18)
	v_mov_b64_e32 v[112:113], v[128:129]
	s_waitcnt vmcnt(17)
	v_mov_b64_e32 v[70:71], v[140:141]
	s_waitcnt vmcnt(16)
	v_mov_b64_e32 v[66:67], v[136:137]
	v_mov_b64_e32 v[188:189], v[78:79]
	v_mov_b64_e32 v[184:185], v[74:75]
	v_mov_b64_e32 v[180:181], v[86:87]
	v_mov_b64_e32 v[176:177], v[82:83]
	v_mov_b64_e32 v[172:173], v[94:95]
	v_mov_b64_e32 v[168:169], v[90:91]
	v_mov_b64_e32 v[164:165], v[102:103]
	v_mov_b64_e32 v[160:161], v[98:99]
	v_mov_b64_e32 v[152:153], v[106:107]
	v_mov_b64_e32 v[148:149], v[124:125]
	v_mov_b64_e32 v[144:145], v[120:121]
	v_mov_b64_e32 v[118:119], v[134:135]
	v_mov_b64_e32 v[114:115], v[130:131]
	v_mov_b64_e32 v[72:73], v[142:143]
	v_mov_b64_e32 v[68:69], v[138:139]
	s_mov_b32 s25, s24
	s_branch .LBB0_1019
